# gather: last group peeled (no redundant row loads), x row and next token's index/gate entries prefetched at the top of the token, epilogue reads prefetched x
# speedup vs baseline: 1.1696x; 1.0047x over previous
.LBB0_1138:
	v_readlane_b32 s8, v254, 40
	v_readlane_b32 s9, v254, 41
	s_add_i32 s2, s2, 1
	s_mov_b64 s[42:43], -1
	s_nop 2
	global_load_dword v0, v97, s[8:9] sc1
	s_waitcnt vmcnt(0)
	v_cmp_ne_u32_e32 vcc, v0, v1
	s_orn2_b64 s[40:41], vcc, exec
	s_branch .LBB0_1135
.Lhop151:
	s_branch .LBB0_151
.LBB0_1139:
	v_readlane_b32 s8, v254, 4
	v_readlane_b32 s9, v254, 5
	s_nop 4
	global_load_dword v0, v97, s[8:9] sc1
	s_waitcnt vmcnt(0)
	v_cmp_eq_u32_e32 vcc, 0, v0
	s_cbranch_vccnz .LBB0_1141
	s_mov_b64 s[42:43], -1
	s_branch .LBB0_1135

.Lgs_done:
	s_waitcnt lgkmcnt(0)
	s_barrier
	s_load_dword s38, s[62:63], 0x0
	s_waitcnt lgkmcnt(0)
	s_lshl_b32 s38, s38, 3
	s_lshl_b32 s0, s44, 9
	v_lshl_add_u32 v26, v80, 2, s0
	global_load_dword v134, v26, s[46:47]
	global_load_dword v135, v26, s[46:47] offset:256
	global_load_dword v136, v26, s[48:49]
	global_load_dword v137, v26, s[48:49] offset:256
	s_waitcnt vmcnt(0)
	s_branch .LBB0_1405

.LBB0_1405:
	s_barrier
	s_waitcnt vmcnt(12)
	v_mov_b32_e32 v18, v134
	v_mov_b32_e32 v16, v135
	v_mov_b32_e32 v19, v136
	v_mov_b32_e32 v17, v137
	s_ashr_i32 s45, s44, 31
	s_lshl_b64 s[0:1], s[44:45], 12
	v_lshl_add_u64 v[100:101], v[84:85], 0, s[0:1]
	v_lshl_add_u64 v[24:25], v[94:95], 0, s[0:1]
	global_load_dwordx4 v[0:3], v[100:101], off offset:48
	global_load_dwordx4 v[4:7], v[100:101], off offset:32
	global_load_dwordx4 v[8:11], v[100:101], off offset:16
	global_load_dwordx4 v[12:15], v[100:101], off
	global_load_dwordx4 v[32:35], v[24:25], off
	global_load_dwordx4 v[138:141], v[24:25], off offset:16
	global_load_dwordx4 v[206:209], v[24:25], off offset:32
	global_load_dwordx4 v[98:101], v[24:25], off offset:48
	s_add_i32 s1, s44, s38
	s_cmpk_lt_i32 s1, 0x4000
	s_cselect_b32 s1, s1, s44
	s_lshl_b32 s0, s1, 9
	v_lshl_add_u32 v26, v80, 2, s0
	global_load_dword v134, v26, s[46:47]
	global_load_dword v135, v26, s[46:47] offset:256
	global_load_dword v136, v26, s[48:49]
	global_load_dword v137, v26, s[48:49] offset:256
	v_lshrrev_b32_e32 v20, 10, v18
	v_lshrrev_b32_e32 v21, 10, v16
	v_mov_b32_e32 v24, 0
	v_cmp_eq_u32_e64 s[8:9], v20, 0
	v_cmp_eq_u32_e64 s[14:15], v21, 0
	s_bcnt1_i32_b64 s2, s[8:9]
	s_bcnt1_i32_b64 s4, s[14:15]
	v_mbcnt_lo_u32_b32 v25, s8, v24
	v_mbcnt_hi_u32_b32 v25, s9, v25
	v_add_u32_e32 v24, s2, v24
	v_cndmask_b32_e64 v22, v22, v25, s[8:9]
	v_mbcnt_lo_u32_b32 v26, s14, v24
	v_mbcnt_hi_u32_b32 v26, s15, v26
	v_add_u32_e32 v24, s4, v24
	v_cndmask_b32_e64 v23, v23, v26, s[14:15]
	v_cmp_eq_u32_e64 s[8:9], v20, 1
	v_cmp_eq_u32_e64 s[14:15], v21, 1
	s_bcnt1_i32_b64 s2, s[8:9]
	s_bcnt1_i32_b64 s4, s[14:15]
	v_mbcnt_lo_u32_b32 v25, s8, v24
	v_mbcnt_hi_u32_b32 v25, s9, v25
	v_add_u32_e32 v24, s2, v24
	v_cndmask_b32_e64 v22, v22, v25, s[8:9]
	v_mbcnt_lo_u32_b32 v26, s14, v24
	v_mbcnt_hi_u32_b32 v26, s15, v26
	v_add_u32_e32 v24, s4, v24
	v_cndmask_b32_e64 v23, v23, v26, s[14:15]
	v_cmp_eq_u32_e64 s[8:9], v20, 2
	v_cmp_eq_u32_e64 s[14:15], v21, 2
	s_bcnt1_i32_b64 s2, s[8:9]
	s_bcnt1_i32_b64 s4, s[14:15]
	v_mbcnt_lo_u32_b32 v25, s8, v24
	v_mbcnt_hi_u32_b32 v25, s9, v25
	v_add_u32_e32 v24, s2, v24
	v_cndmask_b32_e64 v22, v22, v25, s[8:9]
	v_mbcnt_lo_u32_b32 v26, s14, v24
	v_mbcnt_hi_u32_b32 v26, s15, v26
	v_add_u32_e32 v24, s4, v24
	v_cndmask_b32_e64 v23, v23, v26, s[14:15]
	v_cmp_eq_u32_e64 s[8:9], v20, 3
	v_cmp_eq_u32_e64 s[14:15], v21, 3
	s_bcnt1_i32_b64 s2, s[8:9]
	s_bcnt1_i32_b64 s4, s[14:15]
	v_mbcnt_lo_u32_b32 v25, s8, v24
	v_mbcnt_hi_u32_b32 v25, s9, v25
	v_add_u32_e32 v24, s2, v24
	v_cndmask_b32_e64 v22, v22, v25, s[8:9]
	v_mbcnt_lo_u32_b32 v26, s14, v24
	v_mbcnt_hi_u32_b32 v26, s15, v26
	v_add_u32_e32 v24, s4, v24
	v_cndmask_b32_e64 v23, v23, v26, s[14:15]
	v_cmp_eq_u32_e64 s[8:9], v20, 4
	v_cmp_eq_u32_e64 s[14:15], v21, 4
	s_bcnt1_i32_b64 s2, s[8:9]
	s_bcnt1_i32_b64 s4, s[14:15]
	v_mbcnt_lo_u32_b32 v25, s8, v24
	v_mbcnt_hi_u32_b32 v25, s9, v25
	v_add_u32_e32 v24, s2, v24
	v_cndmask_b32_e64 v22, v22, v25, s[8:9]
	v_mbcnt_lo_u32_b32 v26, s14, v24
	v_mbcnt_hi_u32_b32 v26, s15, v26
	v_add_u32_e32 v24, s4, v24
	v_cndmask_b32_e64 v23, v23, v26, s[14:15]
	v_cmp_eq_u32_e64 s[8:9], v20, 5
	v_cmp_eq_u32_e64 s[14:15], v21, 5
	s_bcnt1_i32_b64 s2, s[8:9]
	s_bcnt1_i32_b64 s4, s[14:15]
	v_mbcnt_lo_u32_b32 v25, s8, v24
	v_mbcnt_hi_u32_b32 v25, s9, v25
	v_add_u32_e32 v24, s2, v24
	v_cndmask_b32_e64 v22, v22, v25, s[8:9]
	v_mbcnt_lo_u32_b32 v26, s14, v24
	v_mbcnt_hi_u32_b32 v26, s15, v26
	v_add_u32_e32 v24, s4, v24
	v_cndmask_b32_e64 v23, v23, v26, s[14:15]
	v_cmp_eq_u32_e64 s[8:9], v20, 6
	v_cmp_eq_u32_e64 s[14:15], v21, 6
	s_bcnt1_i32_b64 s2, s[8:9]
	s_bcnt1_i32_b64 s4, s[14:15]
	v_mbcnt_lo_u32_b32 v25, s8, v24
	v_mbcnt_hi_u32_b32 v25, s9, v25
	v_add_u32_e32 v24, s2, v24
	v_cndmask_b32_e64 v22, v22, v25, s[8:9]
	v_mbcnt_lo_u32_b32 v26, s14, v24
	v_mbcnt_hi_u32_b32 v26, s15, v26
	v_add_u32_e32 v24, s4, v24
	v_cndmask_b32_e64 v23, v23, v26, s[14:15]
	v_cmp_eq_u32_e64 s[8:9], v20, 7
	v_cmp_eq_u32_e64 s[14:15], v21, 7
	s_bcnt1_i32_b64 s2, s[8:9]
	s_bcnt1_i32_b64 s4, s[14:15]
	v_mbcnt_lo_u32_b32 v25, s8, v24
	v_mbcnt_hi_u32_b32 v25, s9, v25
	v_add_u32_e32 v24, s2, v24
	v_cndmask_b32_e64 v22, v22, v25, s[8:9]
	v_mbcnt_lo_u32_b32 v26, s14, v24
	v_mbcnt_hi_u32_b32 v26, s15, v26
	v_add_u32_e32 v24, s4, v24
	v_cndmask_b32_e64 v23, v23, v26, s[14:15]
	v_cmp_eq_u32_e64 s[8:9], v20, 8
	v_cmp_eq_u32_e64 s[14:15], v21, 8
	s_bcnt1_i32_b64 s2, s[8:9]
	s_bcnt1_i32_b64 s4, s[14:15]
	v_mbcnt_lo_u32_b32 v25, s8, v24
	v_mbcnt_hi_u32_b32 v25, s9, v25
	v_add_u32_e32 v24, s2, v24
	v_cndmask_b32_e64 v22, v22, v25, s[8:9]
	v_mbcnt_lo_u32_b32 v26, s14, v24
	v_mbcnt_hi_u32_b32 v26, s15, v26
	v_add_u32_e32 v24, s4, v24
	v_cndmask_b32_e64 v23, v23, v26, s[14:15]
	v_cmp_eq_u32_e64 s[8:9], v20, 9
	v_cmp_eq_u32_e64 s[14:15], v21, 9
	s_bcnt1_i32_b64 s2, s[8:9]
	s_bcnt1_i32_b64 s4, s[14:15]
	v_mbcnt_lo_u32_b32 v25, s8, v24
	v_mbcnt_hi_u32_b32 v25, s9, v25
	v_add_u32_e32 v24, s2, v24
	v_cndmask_b32_e64 v22, v22, v25, s[8:9]
	v_mbcnt_lo_u32_b32 v26, s14, v24
	v_mbcnt_hi_u32_b32 v26, s15, v26
	v_add_u32_e32 v24, s4, v24
	v_cndmask_b32_e64 v23, v23, v26, s[14:15]
	v_cmp_eq_u32_e64 s[8:9], v20, 10
	v_cmp_eq_u32_e64 s[14:15], v21, 10
	s_bcnt1_i32_b64 s2, s[8:9]
	s_bcnt1_i32_b64 s4, s[14:15]
	v_mbcnt_lo_u32_b32 v25, s8, v24
	v_mbcnt_hi_u32_b32 v25, s9, v25
	v_add_u32_e32 v24, s2, v24
	v_cndmask_b32_e64 v22, v22, v25, s[8:9]
	v_mbcnt_lo_u32_b32 v26, s14, v24
	v_mbcnt_hi_u32_b32 v26, s15, v26
	v_add_u32_e32 v24, s4, v24
	v_cndmask_b32_e64 v23, v23, v26, s[14:15]
	v_cmp_eq_u32_e64 s[8:9], v20, 11
	v_cmp_eq_u32_e64 s[14:15], v21, 11
	s_bcnt1_i32_b64 s2, s[8:9]
	s_bcnt1_i32_b64 s4, s[14:15]
	v_mbcnt_lo_u32_b32 v25, s8, v24
	v_mbcnt_hi_u32_b32 v25, s9, v25
	v_add_u32_e32 v24, s2, v24
	v_cndmask_b32_e64 v22, v22, v25, s[8:9]
	v_mbcnt_lo_u32_b32 v26, s14, v24
	v_mbcnt_hi_u32_b32 v26, s15, v26
	v_add_u32_e32 v24, s4, v24
	v_cndmask_b32_e64 v23, v23, v26, s[14:15]
	v_cmp_eq_u32_e64 s[8:9], v20, 12
	v_cmp_eq_u32_e64 s[14:15], v21, 12
	s_bcnt1_i32_b64 s2, s[8:9]
	s_bcnt1_i32_b64 s4, s[14:15]
	v_mbcnt_lo_u32_b32 v25, s8, v24
	v_mbcnt_hi_u32_b32 v25, s9, v25
	v_add_u32_e32 v24, s2, v24
	v_cndmask_b32_e64 v22, v22, v25, s[8:9]
	v_mbcnt_lo_u32_b32 v26, s14, v24
	v_mbcnt_hi_u32_b32 v26, s15, v26
	v_add_u32_e32 v24, s4, v24
	v_cndmask_b32_e64 v23, v23, v26, s[14:15]
	v_cmp_eq_u32_e64 s[8:9], v20, 13
	v_cmp_eq_u32_e64 s[14:15], v21, 13
	s_bcnt1_i32_b64 s2, s[8:9]
	s_bcnt1_i32_b64 s4, s[14:15]
	v_mbcnt_lo_u32_b32 v25, s8, v24
	v_mbcnt_hi_u32_b32 v25, s9, v25
	v_add_u32_e32 v24, s2, v24
	v_cndmask_b32_e64 v22, v22, v25, s[8:9]
	v_mbcnt_lo_u32_b32 v26, s14, v24
	v_mbcnt_hi_u32_b32 v26, s15, v26
	v_add_u32_e32 v24, s4, v24
	v_cndmask_b32_e64 v23, v23, v26, s[14:15]
	v_cmp_eq_u32_e64 s[8:9], v20, 14
	v_cmp_eq_u32_e64 s[14:15], v21, 14
	s_bcnt1_i32_b64 s2, s[8:9]
	s_bcnt1_i32_b64 s4, s[14:15]
	v_mbcnt_lo_u32_b32 v25, s8, v24
	v_mbcnt_hi_u32_b32 v25, s9, v25
	v_add_u32_e32 v24, s2, v24
	v_cndmask_b32_e64 v22, v22, v25, s[8:9]
	v_mbcnt_lo_u32_b32 v26, s14, v24
	v_mbcnt_hi_u32_b32 v26, s15, v26
	v_add_u32_e32 v24, s4, v24
	v_cndmask_b32_e64 v23, v23, v26, s[14:15]
	v_cmp_eq_u32_e64 s[8:9], v20, 15
	v_cmp_eq_u32_e64 s[14:15], v21, 15
	s_bcnt1_i32_b64 s2, s[8:9]
	s_bcnt1_i32_b64 s4, s[14:15]
	v_mbcnt_lo_u32_b32 v25, s8, v24
	v_mbcnt_hi_u32_b32 v25, s9, v25
	v_add_u32_e32 v24, s2, v24
	v_cndmask_b32_e64 v22, v22, v25, s[8:9]
	v_mbcnt_lo_u32_b32 v26, s14, v24
	v_mbcnt_hi_u32_b32 v26, s15, v26
	v_add_u32_e32 v24, s4, v24
	v_cndmask_b32_e64 v23, v23, v26, s[14:15]
	v_lshl_add_u32 v250, v22, 3, s21
	v_lshl_add_u32 v251, v23, 3, s21
	ds_write_b64 v250, v[18:19] offset:1024
	ds_write_b64 v251, v[16:17] offset:1024
	v_and_b32_e32 v212, 7, v80
	v_lshl_add_u32 v212, v212, 3, s21
	v_add_u32_e32 v212, 0x400, v212
	v_lshrrev_b32_e32 v213, 4, v80
	v_bfe_u32 v250, v80, 3, 1
	v_lshl_add_u32 v213, v213, 1, v250
	v_lshl_add_u32 v213, v213, 3, s21
	v_add_u32_e32 v213, 0x404, v213
	ds_read_b32 v200, v212
	s_waitcnt vmcnt(8)
	v_lshlrev_b32_e32 v102, 16, v12
	v_and_b32_e32 v103, 0xffff0000, v12
	v_lshlrev_b32_e32 v104, 16, v13
	v_and_b32_e32 v105, 0xffff0000, v13
	v_lshlrev_b32_e32 v106, 16, v14
	v_and_b32_e32 v107, 0xffff0000, v14
	v_lshlrev_b32_e32 v108, 16, v15
	v_and_b32_e32 v109, 0xffff0000, v15
	v_lshlrev_b32_e32 v110, 16, v8
	v_and_b32_e32 v111, 0xffff0000, v8
	v_lshlrev_b32_e32 v112, 16, v9
	v_and_b32_e32 v113, 0xffff0000, v9
	v_lshlrev_b32_e32 v114, 16, v10
	v_and_b32_e32 v115, 0xffff0000, v10
	v_lshlrev_b32_e32 v116, 16, v11
	v_and_b32_e32 v117, 0xffff0000, v11
	v_lshlrev_b32_e32 v118, 16, v4
	v_and_b32_e32 v119, 0xffff0000, v4
	v_lshlrev_b32_e32 v120, 16, v5
	v_and_b32_e32 v121, 0xffff0000, v5
	v_lshlrev_b32_e32 v122, 16, v6
	v_and_b32_e32 v123, 0xffff0000, v6
	v_lshlrev_b32_e32 v124, 16, v7
	v_and_b32_e32 v125, 0xffff0000, v7
	v_lshlrev_b32_e32 v126, 16, v0
	v_and_b32_e32 v127, 0xffff0000, v0
	v_lshlrev_b32_e32 v128, 16, v1
	v_and_b32_e32 v129, 0xffff0000, v1
	v_lshlrev_b32_e32 v130, 16, v2
	v_and_b32_e32 v131, 0xffff0000, v2
	v_lshlrev_b32_e32 v132, 16, v3
	v_and_b32_e32 v133, 0xffff0000, v3
	v_mov_b32_e32 v178, 0
	v_mov_b32_e32 v179, 0
	v_mov_b32_e32 v184, 0
	v_mov_b32_e32 v185, 0
	v_mov_b32_e32 v182, 0
	v_mov_b32_e32 v183, 0
	v_mov_b32_e32 v180, 0
	v_mov_b32_e32 v181, 0
	v_mov_b32_e32 v176, 0
	v_mov_b32_e32 v177, 0
	v_mov_b32_e32 v174, 0
	v_mov_b32_e32 v175, 0
	v_mov_b32_e32 v160, 0
	v_mov_b32_e32 v161, 0
	v_mov_b32_e32 v158, 0
	v_mov_b32_e32 v159, 0
	v_mov_b32_e32 v156, 0
	v_mov_b32_e32 v157, 0
	v_mov_b32_e32 v154, 0
	v_mov_b32_e32 v155, 0
	v_mov_b32_e32 v152, 0
	v_mov_b32_e32 v153, 0
	v_mov_b32_e32 v150, 0
	v_mov_b32_e32 v151, 0
	v_mov_b32_e32 v148, 0
	v_mov_b32_e32 v149, 0
	v_mov_b32_e32 v146, 0
	v_mov_b32_e32 v147, 0
	v_mov_b32_e32 v144, 0
	v_mov_b32_e32 v145, 0
	v_mov_b32_e32 v142, 0
	v_mov_b32_e32 v143, 0
	s_waitcnt lgkmcnt(0)
	v_readlane_b32 s74, v200, 0
	s_lshl_b32 s24, s74, 10
	v_readlane_b32 s74, v200, 1
	s_lshl_b32 s28, s74, 10
	v_readlane_b32 s74, v200, 2
	s_lshl_b32 s29, s74, 10
	v_readlane_b32 s74, v200, 3
	s_lshl_b32 s34, s74, 10
	v_readlane_b32 s74, v200, 4
	s_lshl_b32 s35, s74, 10
	v_readlane_b32 s74, v200, 5
	s_lshl_b32 s42, s74, 10
	v_readlane_b32 s74, v200, 6
	s_lshl_b32 s43, s74, 10
	v_readlane_b32 s74, v200, 7
	s_lshl_b32 s50, s74, 10
	s_add_u32 s0, s93, s24
	s_addc_u32 s1, s20, 0
	global_load_dwordx4 v[0:3], v81, s[0:1]
	s_add_u32 s4, s93, s28
	s_addc_u32 s5, s20, 0
	global_load_dwordx4 v[4:7], v81, s[4:5]
	s_add_u32 s0, s93, s29
	s_addc_u32 s1, s20, 0
	global_load_dwordx4 v[8:11], v81, s[0:1]
	s_add_u32 s4, s93, s34
	s_addc_u32 s5, s20, 0
	global_load_dwordx4 v[12:15], v81, s[4:5]
	s_add_u32 s0, s93, s35
	s_addc_u32 s1, s20, 0
	global_load_dwordx4 v[16:19], v81, s[0:1]
	s_add_u32 s4, s93, s42
	s_addc_u32 s5, s20, 0
	global_load_dwordx4 v[20:23], v81, s[4:5]
	s_add_u32 s0, s93, s43
	s_addc_u32 s1, s20, 0
	global_load_dwordx4 v[24:27], v81, s[0:1]
	s_add_u32 s4, s93, s50
	s_addc_u32 s5, s20, 0
	global_load_dwordx4 v[28:31], v81, s[4:5]
	s_add_u32 s0, s89, s24
	s_addc_u32 s1, s92, 0
	global_load_dwordx4 v[36:39], v81, s[0:1]
	s_add_u32 s4, s89, s28
	s_addc_u32 s5, s92, 0
	global_load_dwordx4 v[40:43], v81, s[4:5]
	s_lshr_b32 s8, s24, 6
	s_add_u32 s8, s6, s8
	s_addc_u32 s9, s88, 0
	global_load_dword v68, v83, s[8:9]
	s_lshr_b32 s14, s28, 6
	s_add_u32 s14, s6, s14
	s_addc_u32 s15, s88, 0
	global_load_dword v69, v83, s[14:15]
	s_add_u32 s0, s89, s29
	s_addc_u32 s1, s92, 0
	global_load_dwordx4 v[44:47], v81, s[0:1]
	s_add_u32 s4, s89, s34
	s_addc_u32 s5, s92, 0
	global_load_dwordx4 v[48:51], v81, s[4:5]
	s_lshr_b32 s8, s29, 6
	s_add_u32 s8, s6, s8
	s_addc_u32 s9, s88, 0
	global_load_dword v70, v83, s[8:9]
	s_lshr_b32 s14, s34, 6
	s_add_u32 s14, s6, s14
	s_addc_u32 s15, s88, 0
	global_load_dword v71, v83, s[14:15]
	s_add_u32 s0, s89, s35
	s_addc_u32 s1, s92, 0
	global_load_dwordx4 v[52:55], v81, s[0:1]
	s_add_u32 s4, s89, s42
	s_addc_u32 s5, s92, 0
	global_load_dwordx4 v[56:59], v81, s[4:5]
	s_lshr_b32 s8, s35, 6
	s_add_u32 s8, s6, s8
	s_addc_u32 s9, s88, 0
	global_load_dword v72, v83, s[8:9]
	s_lshr_b32 s14, s42, 6
	s_add_u32 s14, s6, s14
	s_addc_u32 s15, s88, 0
	global_load_dword v73, v83, s[14:15]
	s_add_u32 s0, s89, s43
	s_addc_u32 s1, s92, 0
	global_load_dwordx4 v[60:63], v81, s[0:1]
	s_add_u32 s4, s89, s50
	s_addc_u32 s5, s92, 0
	global_load_dwordx4 v[64:67], v81, s[4:5]
	s_lshr_b32 s8, s43, 6
	s_add_u32 s8, s6, s8
	s_addc_u32 s9, s88, 0
	global_load_dword v74, v83, s[8:9]
	s_lshr_b32 s14, s50, 6
	s_add_u32 s14, s6, s14
	s_addc_u32 s15, s88, 0
	global_load_dword v75, v83, s[14:15]
	s_mov_b32 s2, 0
.Lgm_loop:
	s_add_i32 s0, s2, 64
	v_add_u32_e32 v250, s0, v212
	ds_read_b32 v200, v250
	v_add_u32_e32 v251, s2, v213
	ds_read_b32 v201, v251
	s_waitcnt vmcnt(22)
	v_cvt_scalef32_pk_f32_fp4 v[228:229], v0, 1.0
	v_cvt_scalef32_pk_f32_fp4 v[230:231], v0, 1.0 op_sel:[1,0,0]
	v_cvt_scalef32_pk_f32_fp4 v[232:233], v0, 1.0 op_sel:[0,1,0]
	v_cvt_scalef32_pk_f32_fp4 v[234:235], v0, 1.0 op_sel:[1,1,0]
	v_cvt_scalef32_pk_f32_fp4 v[236:237], v4, 1.0
	v_cvt_scalef32_pk_f32_fp4 v[238:239], v4, 1.0 op_sel:[1,0,0]
	v_cvt_scalef32_pk_f32_fp4 v[240:241], v4, 1.0 op_sel:[0,1,0]
	v_cvt_scalef32_pk_f32_fp4 v[242:243], v4, 1.0 op_sel:[1,1,0]
	v_pk_mul_f32 v[244:245], v[228:229], v[102:103]
	v_pk_mul_f32 v[246:247], v[236:237], v[102:103]
	v_pk_fma_f32 v[244:245], v[230:231], v[104:105], v[244:245]
	v_pk_fma_f32 v[246:247], v[238:239], v[104:105], v[246:247]
	v_pk_fma_f32 v[244:245], v[232:233], v[106:107], v[244:245]
	v_pk_fma_f32 v[246:247], v[240:241], v[106:107], v[246:247]
	v_pk_fma_f32 v[244:245], v[234:235], v[108:109], v[244:245]
	v_pk_fma_f32 v[246:247], v[242:243], v[108:109], v[246:247]
	v_cvt_scalef32_pk_f32_fp4 v[228:229], v1, 1.0
	v_cvt_scalef32_pk_f32_fp4 v[230:231], v1, 1.0 op_sel:[1,0,0]
	v_cvt_scalef32_pk_f32_fp4 v[232:233], v1, 1.0 op_sel:[0,1,0]
	v_cvt_scalef32_pk_f32_fp4 v[234:235], v1, 1.0 op_sel:[1,1,0]
	v_cvt_scalef32_pk_f32_fp4 v[236:237], v5, 1.0
	v_cvt_scalef32_pk_f32_fp4 v[238:239], v5, 1.0 op_sel:[1,0,0]
	v_cvt_scalef32_pk_f32_fp4 v[240:241], v5, 1.0 op_sel:[0,1,0]
	v_cvt_scalef32_pk_f32_fp4 v[242:243], v5, 1.0 op_sel:[1,1,0]
	v_pk_fma_f32 v[244:245], v[228:229], v[110:111], v[244:245]
	v_pk_fma_f32 v[246:247], v[236:237], v[110:111], v[246:247]
	v_pk_fma_f32 v[244:245], v[230:231], v[112:113], v[244:245]
	v_pk_fma_f32 v[246:247], v[238:239], v[112:113], v[246:247]
	v_pk_fma_f32 v[244:245], v[232:233], v[114:115], v[244:245]
	v_pk_fma_f32 v[246:247], v[240:241], v[114:115], v[246:247]
	v_pk_fma_f32 v[244:245], v[234:235], v[116:117], v[244:245]
	v_pk_fma_f32 v[246:247], v[242:243], v[116:117], v[246:247]
	v_cvt_scalef32_pk_f32_fp4 v[228:229], v2, 1.0
	v_cvt_scalef32_pk_f32_fp4 v[230:231], v2, 1.0 op_sel:[1,0,0]
	v_cvt_scalef32_pk_f32_fp4 v[232:233], v2, 1.0 op_sel:[0,1,0]
	v_cvt_scalef32_pk_f32_fp4 v[234:235], v2, 1.0 op_sel:[1,1,0]
	v_cvt_scalef32_pk_f32_fp4 v[236:237], v6, 1.0
	v_cvt_scalef32_pk_f32_fp4 v[238:239], v6, 1.0 op_sel:[1,0,0]
	v_cvt_scalef32_pk_f32_fp4 v[240:241], v6, 1.0 op_sel:[0,1,0]
	v_cvt_scalef32_pk_f32_fp4 v[242:243], v6, 1.0 op_sel:[1,1,0]
	v_pk_fma_f32 v[244:245], v[228:229], v[118:119], v[244:245]
	v_pk_fma_f32 v[246:247], v[236:237], v[118:119], v[246:247]
	v_pk_fma_f32 v[244:245], v[230:231], v[120:121], v[244:245]
	v_pk_fma_f32 v[246:247], v[238:239], v[120:121], v[246:247]
	v_pk_fma_f32 v[244:245], v[232:233], v[122:123], v[244:245]
	v_pk_fma_f32 v[246:247], v[240:241], v[122:123], v[246:247]
	v_pk_fma_f32 v[244:245], v[234:235], v[124:125], v[244:245]
	v_pk_fma_f32 v[246:247], v[242:243], v[124:125], v[246:247]
	v_cvt_scalef32_pk_f32_fp4 v[228:229], v3, 1.0
	v_cvt_scalef32_pk_f32_fp4 v[230:231], v3, 1.0 op_sel:[1,0,0]
	v_cvt_scalef32_pk_f32_fp4 v[232:233], v3, 1.0 op_sel:[0,1,0]
	v_cvt_scalef32_pk_f32_fp4 v[234:235], v3, 1.0 op_sel:[1,1,0]
	v_cvt_scalef32_pk_f32_fp4 v[236:237], v7, 1.0
	v_cvt_scalef32_pk_f32_fp4 v[238:239], v7, 1.0 op_sel:[1,0,0]
	v_cvt_scalef32_pk_f32_fp4 v[240:241], v7, 1.0 op_sel:[0,1,0]
	v_cvt_scalef32_pk_f32_fp4 v[242:243], v7, 1.0 op_sel:[1,1,0]
	v_pk_fma_f32 v[244:245], v[228:229], v[126:127], v[244:245]
	v_pk_fma_f32 v[246:247], v[236:237], v[126:127], v[246:247]
	v_pk_fma_f32 v[244:245], v[230:231], v[128:129], v[244:245]
	v_pk_fma_f32 v[246:247], v[238:239], v[128:129], v[246:247]
	v_pk_fma_f32 v[244:245], v[232:233], v[130:131], v[244:245]
	v_pk_fma_f32 v[246:247], v[240:241], v[130:131], v[246:247]
	v_pk_fma_f32 v[244:245], v[234:235], v[132:133], v[244:245]
	v_pk_fma_f32 v[246:247], v[242:243], v[132:133], v[246:247]
	v_add_f32_e32 v186, v244, v245
	v_add_f32_e32 v187, v246, v247
	s_waitcnt lgkmcnt(0)
	v_readlane_b32 s74, v200, 0
	s_lshl_b32 s24, s74, 10
	v_readlane_b32 s74, v200, 1
	s_lshl_b32 s28, s74, 10
	v_readlane_b32 s74, v200, 2
	s_lshl_b32 s29, s74, 10
	v_readlane_b32 s74, v200, 3
	s_lshl_b32 s34, s74, 10
	v_readlane_b32 s74, v200, 4
	s_lshl_b32 s35, s74, 10
	v_readlane_b32 s74, v200, 5
	s_lshl_b32 s42, s74, 10
	v_readlane_b32 s74, v200, 6
	s_lshl_b32 s43, s74, 10
	v_readlane_b32 s74, v200, 7
	s_lshl_b32 s50, s74, 10
	s_add_u32 s0, s93, s24
	s_addc_u32 s1, s20, 0
	global_load_dwordx4 v[0:3], v81, s[0:1]
	s_add_u32 s4, s93, s28
	s_addc_u32 s5, s20, 0
	global_load_dwordx4 v[4:7], v81, s[4:5]
	s_waitcnt vmcnt(22)
	v_cvt_scalef32_pk_f32_fp4 v[228:229], v8, 1.0
	v_cvt_scalef32_pk_f32_fp4 v[230:231], v8, 1.0 op_sel:[1,0,0]
	v_cvt_scalef32_pk_f32_fp4 v[232:233], v8, 1.0 op_sel:[0,1,0]
	v_cvt_scalef32_pk_f32_fp4 v[234:235], v8, 1.0 op_sel:[1,1,0]
	v_cvt_scalef32_pk_f32_fp4 v[236:237], v12, 1.0
	v_cvt_scalef32_pk_f32_fp4 v[238:239], v12, 1.0 op_sel:[1,0,0]
	v_cvt_scalef32_pk_f32_fp4 v[240:241], v12, 1.0 op_sel:[0,1,0]
	v_cvt_scalef32_pk_f32_fp4 v[242:243], v12, 1.0 op_sel:[1,1,0]
	v_pk_mul_f32 v[244:245], v[228:229], v[102:103]
	v_pk_mul_f32 v[246:247], v[236:237], v[102:103]
	v_pk_fma_f32 v[244:245], v[230:231], v[104:105], v[244:245]
	v_pk_fma_f32 v[246:247], v[238:239], v[104:105], v[246:247]
	v_pk_fma_f32 v[244:245], v[232:233], v[106:107], v[244:245]
	v_pk_fma_f32 v[246:247], v[240:241], v[106:107], v[246:247]
	v_pk_fma_f32 v[244:245], v[234:235], v[108:109], v[244:245]
	v_pk_fma_f32 v[246:247], v[242:243], v[108:109], v[246:247]
	v_cvt_scalef32_pk_f32_fp4 v[228:229], v9, 1.0
	v_cvt_scalef32_pk_f32_fp4 v[230:231], v9, 1.0 op_sel:[1,0,0]
	v_cvt_scalef32_pk_f32_fp4 v[232:233], v9, 1.0 op_sel:[0,1,0]
	v_cvt_scalef32_pk_f32_fp4 v[234:235], v9, 1.0 op_sel:[1,1,0]
	v_cvt_scalef32_pk_f32_fp4 v[236:237], v13, 1.0
	v_cvt_scalef32_pk_f32_fp4 v[238:239], v13, 1.0 op_sel:[1,0,0]
	v_cvt_scalef32_pk_f32_fp4 v[240:241], v13, 1.0 op_sel:[0,1,0]
	v_cvt_scalef32_pk_f32_fp4 v[242:243], v13, 1.0 op_sel:[1,1,0]
	v_pk_fma_f32 v[244:245], v[228:229], v[110:111], v[244:245]
	v_pk_fma_f32 v[246:247], v[236:237], v[110:111], v[246:247]
	v_pk_fma_f32 v[244:245], v[230:231], v[112:113], v[244:245]
	v_pk_fma_f32 v[246:247], v[238:239], v[112:113], v[246:247]
	v_pk_fma_f32 v[244:245], v[232:233], v[114:115], v[244:245]
	v_pk_fma_f32 v[246:247], v[240:241], v[114:115], v[246:247]
	v_pk_fma_f32 v[244:245], v[234:235], v[116:117], v[244:245]
	v_pk_fma_f32 v[246:247], v[242:243], v[116:117], v[246:247]
	v_cvt_scalef32_pk_f32_fp4 v[228:229], v10, 1.0
	v_cvt_scalef32_pk_f32_fp4 v[230:231], v10, 1.0 op_sel:[1,0,0]
	v_cvt_scalef32_pk_f32_fp4 v[232:233], v10, 1.0 op_sel:[0,1,0]
	v_cvt_scalef32_pk_f32_fp4 v[234:235], v10, 1.0 op_sel:[1,1,0]
	v_cvt_scalef32_pk_f32_fp4 v[236:237], v14, 1.0
	v_cvt_scalef32_pk_f32_fp4 v[238:239], v14, 1.0 op_sel:[1,0,0]
	v_cvt_scalef32_pk_f32_fp4 v[240:241], v14, 1.0 op_sel:[0,1,0]
	v_cvt_scalef32_pk_f32_fp4 v[242:243], v14, 1.0 op_sel:[1,1,0]
	v_pk_fma_f32 v[244:245], v[228:229], v[118:119], v[244:245]
	v_pk_fma_f32 v[246:247], v[236:237], v[118:119], v[246:247]
	v_pk_fma_f32 v[244:245], v[230:231], v[120:121], v[244:245]
	v_pk_fma_f32 v[246:247], v[238:239], v[120:121], v[246:247]
	v_pk_fma_f32 v[244:245], v[232:233], v[122:123], v[244:245]
	v_pk_fma_f32 v[246:247], v[240:241], v[122:123], v[246:247]
	v_pk_fma_f32 v[244:245], v[234:235], v[124:125], v[244:245]
	v_pk_fma_f32 v[246:247], v[242:243], v[124:125], v[246:247]
	v_cvt_scalef32_pk_f32_fp4 v[228:229], v11, 1.0
	v_cvt_scalef32_pk_f32_fp4 v[230:231], v11, 1.0 op_sel:[1,0,0]
	v_cvt_scalef32_pk_f32_fp4 v[232:233], v11, 1.0 op_sel:[0,1,0]
	v_cvt_scalef32_pk_f32_fp4 v[234:235], v11, 1.0 op_sel:[1,1,0]
	v_cvt_scalef32_pk_f32_fp4 v[236:237], v15, 1.0
	v_cvt_scalef32_pk_f32_fp4 v[238:239], v15, 1.0 op_sel:[1,0,0]
	v_cvt_scalef32_pk_f32_fp4 v[240:241], v15, 1.0 op_sel:[0,1,0]
	v_cvt_scalef32_pk_f32_fp4 v[242:243], v15, 1.0 op_sel:[1,1,0]
	v_pk_fma_f32 v[244:245], v[228:229], v[126:127], v[244:245]
	v_pk_fma_f32 v[246:247], v[236:237], v[126:127], v[246:247]
	v_pk_fma_f32 v[244:245], v[230:231], v[128:129], v[244:245]
	v_pk_fma_f32 v[246:247], v[238:239], v[128:129], v[246:247]
	v_pk_fma_f32 v[244:245], v[232:233], v[130:131], v[244:245]
	v_pk_fma_f32 v[246:247], v[240:241], v[130:131], v[246:247]
	v_pk_fma_f32 v[244:245], v[234:235], v[132:133], v[244:245]
	v_pk_fma_f32 v[246:247], v[242:243], v[132:133], v[246:247]
	v_add_f32_e32 v188, v244, v245
	v_add_f32_e32 v189, v246, v247
	s_add_u32 s0, s93, s29
	s_addc_u32 s1, s20, 0
	global_load_dwordx4 v[8:11], v81, s[0:1]
	s_add_u32 s4, s93, s34
	s_addc_u32 s5, s20, 0
	global_load_dwordx4 v[12:15], v81, s[4:5]
	s_waitcnt vmcnt(22)
	v_cvt_scalef32_pk_f32_fp4 v[228:229], v16, 1.0
	v_cvt_scalef32_pk_f32_fp4 v[230:231], v16, 1.0 op_sel:[1,0,0]
	v_cvt_scalef32_pk_f32_fp4 v[232:233], v16, 1.0 op_sel:[0,1,0]
	v_cvt_scalef32_pk_f32_fp4 v[234:235], v16, 1.0 op_sel:[1,1,0]
	v_cvt_scalef32_pk_f32_fp4 v[236:237], v20, 1.0
	v_cvt_scalef32_pk_f32_fp4 v[238:239], v20, 1.0 op_sel:[1,0,0]
	v_cvt_scalef32_pk_f32_fp4 v[240:241], v20, 1.0 op_sel:[0,1,0]
	v_cvt_scalef32_pk_f32_fp4 v[242:243], v20, 1.0 op_sel:[1,1,0]
	v_pk_mul_f32 v[244:245], v[228:229], v[102:103]
	v_pk_mul_f32 v[246:247], v[236:237], v[102:103]
	v_pk_fma_f32 v[244:245], v[230:231], v[104:105], v[244:245]
	v_pk_fma_f32 v[246:247], v[238:239], v[104:105], v[246:247]
	v_pk_fma_f32 v[244:245], v[232:233], v[106:107], v[244:245]
	v_pk_fma_f32 v[246:247], v[240:241], v[106:107], v[246:247]
	v_pk_fma_f32 v[244:245], v[234:235], v[108:109], v[244:245]
	v_pk_fma_f32 v[246:247], v[242:243], v[108:109], v[246:247]
	v_cvt_scalef32_pk_f32_fp4 v[228:229], v17, 1.0
	v_cvt_scalef32_pk_f32_fp4 v[230:231], v17, 1.0 op_sel:[1,0,0]
	v_cvt_scalef32_pk_f32_fp4 v[232:233], v17, 1.0 op_sel:[0,1,0]
	v_cvt_scalef32_pk_f32_fp4 v[234:235], v17, 1.0 op_sel:[1,1,0]
	v_cvt_scalef32_pk_f32_fp4 v[236:237], v21, 1.0
	v_cvt_scalef32_pk_f32_fp4 v[238:239], v21, 1.0 op_sel:[1,0,0]
	v_cvt_scalef32_pk_f32_fp4 v[240:241], v21, 1.0 op_sel:[0,1,0]
	v_cvt_scalef32_pk_f32_fp4 v[242:243], v21, 1.0 op_sel:[1,1,0]
	v_pk_fma_f32 v[244:245], v[228:229], v[110:111], v[244:245]
	v_pk_fma_f32 v[246:247], v[236:237], v[110:111], v[246:247]
	v_pk_fma_f32 v[244:245], v[230:231], v[112:113], v[244:245]
	v_pk_fma_f32 v[246:247], v[238:239], v[112:113], v[246:247]
	v_pk_fma_f32 v[244:245], v[232:233], v[114:115], v[244:245]
	v_pk_fma_f32 v[246:247], v[240:241], v[114:115], v[246:247]
	v_pk_fma_f32 v[244:245], v[234:235], v[116:117], v[244:245]
	v_pk_fma_f32 v[246:247], v[242:243], v[116:117], v[246:247]
	v_cvt_scalef32_pk_f32_fp4 v[228:229], v18, 1.0
	v_cvt_scalef32_pk_f32_fp4 v[230:231], v18, 1.0 op_sel:[1,0,0]
	v_cvt_scalef32_pk_f32_fp4 v[232:233], v18, 1.0 op_sel:[0,1,0]
	v_cvt_scalef32_pk_f32_fp4 v[234:235], v18, 1.0 op_sel:[1,1,0]
	v_cvt_scalef32_pk_f32_fp4 v[236:237], v22, 1.0
	v_cvt_scalef32_pk_f32_fp4 v[238:239], v22, 1.0 op_sel:[1,0,0]
	v_cvt_scalef32_pk_f32_fp4 v[240:241], v22, 1.0 op_sel:[0,1,0]
	v_cvt_scalef32_pk_f32_fp4 v[242:243], v22, 1.0 op_sel:[1,1,0]
	v_pk_fma_f32 v[244:245], v[228:229], v[118:119], v[244:245]
	v_pk_fma_f32 v[246:247], v[236:237], v[118:119], v[246:247]
	v_pk_fma_f32 v[244:245], v[230:231], v[120:121], v[244:245]
	v_pk_fma_f32 v[246:247], v[238:239], v[120:121], v[246:247]
	v_pk_fma_f32 v[244:245], v[232:233], v[122:123], v[244:245]
	v_pk_fma_f32 v[246:247], v[240:241], v[122:123], v[246:247]
	v_pk_fma_f32 v[244:245], v[234:235], v[124:125], v[244:245]
	v_pk_fma_f32 v[246:247], v[242:243], v[124:125], v[246:247]
	v_cvt_scalef32_pk_f32_fp4 v[228:229], v19, 1.0
	v_cvt_scalef32_pk_f32_fp4 v[230:231], v19, 1.0 op_sel:[1,0,0]
	v_cvt_scalef32_pk_f32_fp4 v[232:233], v19, 1.0 op_sel:[0,1,0]
	v_cvt_scalef32_pk_f32_fp4 v[234:235], v19, 1.0 op_sel:[1,1,0]
	v_cvt_scalef32_pk_f32_fp4 v[236:237], v23, 1.0
	v_cvt_scalef32_pk_f32_fp4 v[238:239], v23, 1.0 op_sel:[1,0,0]
	v_cvt_scalef32_pk_f32_fp4 v[240:241], v23, 1.0 op_sel:[0,1,0]
	v_cvt_scalef32_pk_f32_fp4 v[242:243], v23, 1.0 op_sel:[1,1,0]
	v_pk_fma_f32 v[244:245], v[228:229], v[126:127], v[244:245]
	v_pk_fma_f32 v[246:247], v[236:237], v[126:127], v[246:247]
	v_pk_fma_f32 v[244:245], v[230:231], v[128:129], v[244:245]
	v_pk_fma_f32 v[246:247], v[238:239], v[128:129], v[246:247]
	v_pk_fma_f32 v[244:245], v[232:233], v[130:131], v[244:245]
	v_pk_fma_f32 v[246:247], v[240:241], v[130:131], v[246:247]
	v_pk_fma_f32 v[244:245], v[234:235], v[132:133], v[244:245]
	v_pk_fma_f32 v[246:247], v[242:243], v[132:133], v[246:247]
	v_add_f32_e32 v190, v244, v245
	v_add_f32_e32 v191, v246, v247
	s_add_u32 s0, s93, s35
	s_addc_u32 s1, s20, 0
	global_load_dwordx4 v[16:19], v81, s[0:1]
	s_add_u32 s4, s93, s42
	s_addc_u32 s5, s20, 0
	global_load_dwordx4 v[20:23], v81, s[4:5]
	s_waitcnt vmcnt(22)
	v_cvt_scalef32_pk_f32_fp4 v[228:229], v24, 1.0
	v_cvt_scalef32_pk_f32_fp4 v[230:231], v24, 1.0 op_sel:[1,0,0]
	v_cvt_scalef32_pk_f32_fp4 v[232:233], v24, 1.0 op_sel:[0,1,0]
	v_cvt_scalef32_pk_f32_fp4 v[234:235], v24, 1.0 op_sel:[1,1,0]
	v_cvt_scalef32_pk_f32_fp4 v[236:237], v28, 1.0
	v_cvt_scalef32_pk_f32_fp4 v[238:239], v28, 1.0 op_sel:[1,0,0]
	v_cvt_scalef32_pk_f32_fp4 v[240:241], v28, 1.0 op_sel:[0,1,0]
	v_cvt_scalef32_pk_f32_fp4 v[242:243], v28, 1.0 op_sel:[1,1,0]
	v_pk_mul_f32 v[244:245], v[228:229], v[102:103]
	v_pk_mul_f32 v[246:247], v[236:237], v[102:103]
	v_pk_fma_f32 v[244:245], v[230:231], v[104:105], v[244:245]
	v_pk_fma_f32 v[246:247], v[238:239], v[104:105], v[246:247]
	v_pk_fma_f32 v[244:245], v[232:233], v[106:107], v[244:245]
	v_pk_fma_f32 v[246:247], v[240:241], v[106:107], v[246:247]
	v_pk_fma_f32 v[244:245], v[234:235], v[108:109], v[244:245]
	v_pk_fma_f32 v[246:247], v[242:243], v[108:109], v[246:247]
	v_cvt_scalef32_pk_f32_fp4 v[228:229], v25, 1.0
	v_cvt_scalef32_pk_f32_fp4 v[230:231], v25, 1.0 op_sel:[1,0,0]
	v_cvt_scalef32_pk_f32_fp4 v[232:233], v25, 1.0 op_sel:[0,1,0]
	v_cvt_scalef32_pk_f32_fp4 v[234:235], v25, 1.0 op_sel:[1,1,0]
	v_cvt_scalef32_pk_f32_fp4 v[236:237], v29, 1.0
	v_cvt_scalef32_pk_f32_fp4 v[238:239], v29, 1.0 op_sel:[1,0,0]
	v_cvt_scalef32_pk_f32_fp4 v[240:241], v29, 1.0 op_sel:[0,1,0]
	v_cvt_scalef32_pk_f32_fp4 v[242:243], v29, 1.0 op_sel:[1,1,0]
	v_pk_fma_f32 v[244:245], v[228:229], v[110:111], v[244:245]
	v_pk_fma_f32 v[246:247], v[236:237], v[110:111], v[246:247]
	v_pk_fma_f32 v[244:245], v[230:231], v[112:113], v[244:245]
	v_pk_fma_f32 v[246:247], v[238:239], v[112:113], v[246:247]
	v_pk_fma_f32 v[244:245], v[232:233], v[114:115], v[244:245]
	v_pk_fma_f32 v[246:247], v[240:241], v[114:115], v[246:247]
	v_pk_fma_f32 v[244:245], v[234:235], v[116:117], v[244:245]
	v_pk_fma_f32 v[246:247], v[242:243], v[116:117], v[246:247]
	v_cvt_scalef32_pk_f32_fp4 v[228:229], v26, 1.0
	v_cvt_scalef32_pk_f32_fp4 v[230:231], v26, 1.0 op_sel:[1,0,0]
	v_cvt_scalef32_pk_f32_fp4 v[232:233], v26, 1.0 op_sel:[0,1,0]
	v_cvt_scalef32_pk_f32_fp4 v[234:235], v26, 1.0 op_sel:[1,1,0]
	v_cvt_scalef32_pk_f32_fp4 v[236:237], v30, 1.0
	v_cvt_scalef32_pk_f32_fp4 v[238:239], v30, 1.0 op_sel:[1,0,0]
	v_cvt_scalef32_pk_f32_fp4 v[240:241], v30, 1.0 op_sel:[0,1,0]
	v_cvt_scalef32_pk_f32_fp4 v[242:243], v30, 1.0 op_sel:[1,1,0]
	v_pk_fma_f32 v[244:245], v[228:229], v[118:119], v[244:245]
	v_pk_fma_f32 v[246:247], v[236:237], v[118:119], v[246:247]
	v_pk_fma_f32 v[244:245], v[230:231], v[120:121], v[244:245]
	v_pk_fma_f32 v[246:247], v[238:239], v[120:121], v[246:247]
	v_pk_fma_f32 v[244:245], v[232:233], v[122:123], v[244:245]
	v_pk_fma_f32 v[246:247], v[240:241], v[122:123], v[246:247]
	v_pk_fma_f32 v[244:245], v[234:235], v[124:125], v[244:245]
	v_pk_fma_f32 v[246:247], v[242:243], v[124:125], v[246:247]
	v_cvt_scalef32_pk_f32_fp4 v[228:229], v27, 1.0
	v_cvt_scalef32_pk_f32_fp4 v[230:231], v27, 1.0 op_sel:[1,0,0]
	v_cvt_scalef32_pk_f32_fp4 v[232:233], v27, 1.0 op_sel:[0,1,0]
	v_cvt_scalef32_pk_f32_fp4 v[234:235], v27, 1.0 op_sel:[1,1,0]
	v_cvt_scalef32_pk_f32_fp4 v[236:237], v31, 1.0
	v_cvt_scalef32_pk_f32_fp4 v[238:239], v31, 1.0 op_sel:[1,0,0]
	v_cvt_scalef32_pk_f32_fp4 v[240:241], v31, 1.0 op_sel:[0,1,0]
	v_cvt_scalef32_pk_f32_fp4 v[242:243], v31, 1.0 op_sel:[1,1,0]
	v_pk_fma_f32 v[244:245], v[228:229], v[126:127], v[244:245]
	v_pk_fma_f32 v[246:247], v[236:237], v[126:127], v[246:247]
	v_pk_fma_f32 v[244:245], v[230:231], v[128:129], v[244:245]
	v_pk_fma_f32 v[246:247], v[238:239], v[128:129], v[246:247]
	v_pk_fma_f32 v[244:245], v[232:233], v[130:131], v[244:245]
	v_pk_fma_f32 v[246:247], v[240:241], v[130:131], v[246:247]
	v_pk_fma_f32 v[244:245], v[234:235], v[132:133], v[244:245]
	v_pk_fma_f32 v[246:247], v[242:243], v[132:133], v[246:247]
	v_add_f32_e32 v192, v244, v245
	v_add_f32_e32 v193, v246, v247
	s_add_u32 s0, s93, s43
	s_addc_u32 s1, s20, 0
	global_load_dwordx4 v[24:27], v81, s[0:1]
	s_add_u32 s4, s93, s50
	s_addc_u32 s5, s20, 0
	global_load_dwordx4 v[28:31], v81, s[4:5]
	s_waitcnt vmcnt(8)
	v_lshlrev_b32_e32 v76, 16, v68
	v_mul_f32_e32 v186, v186, v76
	v_lshlrev_b32_e32 v77, 16, v69
	v_mul_f32_e32 v187, v187, v77
	v_lshlrev_b32_e32 v76, 16, v70
	v_mul_f32_e32 v188, v188, v76
	v_lshlrev_b32_e32 v77, 16, v71
	v_mul_f32_e32 v189, v189, v77
	v_lshlrev_b32_e32 v76, 16, v72
	v_mul_f32_e32 v190, v190, v76
	v_lshlrev_b32_e32 v77, 16, v73
	v_mul_f32_e32 v191, v191, v77
	v_lshlrev_b32_e32 v76, 16, v74
	v_mul_f32_e32 v192, v192, v76
	v_lshlrev_b32_e32 v77, 16, v75
	v_mul_f32_e32 v193, v193, v77
	s_nop 1
	v_permlane32_swap_b32_e32 v186, v190
	v_permlane32_swap_b32_e32 v187, v191
	v_permlane32_swap_b32_e32 v188, v192
	v_permlane32_swap_b32_e32 v189, v193
	s_nop 0
	v_add_f32_e32 v186, v186, v190
	v_add_f32_e32 v187, v187, v191
	v_add_f32_e32 v188, v188, v192
	v_add_f32_e32 v189, v189, v193
	s_nop 1
	v_permlane16_swap_b32_e32 v186, v188
	v_permlane16_swap_b32_e32 v187, v189
	s_nop 0
	v_add_f32_e32 v186, v186, v188
	v_add_f32_e32 v187, v187, v189
	s_nop 1
	v_add_f32_dpp v248, v186, v186 row_ror:8 row_mask:0xf bank_mask:0x3
	v_add_f32_dpp v248, v187, v187 row_ror:8 row_mask:0xf bank_mask:0xc
	s_nop 1
	v_add_f32_dpp v248, v248, v248 quad_perm:[1,0,3,2] row_mask:0xf bank_mask:0xf
	s_nop 1
	v_add_f32_dpp v248, v248, v248 quad_perm:[2,3,0,1] row_mask:0xf bank_mask:0xf
	s_nop 1
	v_add_f32_dpp v248, v248, v248 row_half_mirror row_mask:0xf bank_mask:0xf
	v_fma_f32 v202, |v248|, s57, 1.0
	v_mul_f32_e32 v204, v248, v248
	v_rcp_f32_e32 v202, v202
	v_mul_f32_e32 v204, 0xbf38aa3b, v204
	v_cmp_gt_f32_e32 vcc, 0, v248
	v_exp_f32_e32 v204, v204
	v_fmamk_f32 v203, v202, 0x3f07dc22, v216
	v_fmaak_f32 v203, v203, v202, 0x3f35f0e3
	v_fmaak_f32 v203, v203, v202, 0xbe11a98e
	v_fmaak_f32 v203, v203, v202, 0x3e027906
	v_mul_f32_e32 v202, v202, v203
	v_mul_f32_e32 v202, v204, v202
	v_mul_f32_e32 v203, v248, v202
	v_fma_f32 v204, -v248, v202, v248
	v_cndmask_b32_e32 v204, v204, v203, vcc
	v_mul_f32_e32 v204, v201, v204
	s_nop 1
	v_readlane_b32 s51, v204, 0
	v_readlane_b32 s64, v204, 8
	v_readlane_b32 s65, v204, 16
	v_readlane_b32 s78, v204, 24
	v_readlane_b32 s79, v204, 32
	v_readlane_b32 s82, v204, 40
	v_readlane_b32 s84, v204, 48
	v_readlane_b32 s10, v204, 56
	s_waitcnt vmcnt(22)
	v_and_b32_e32 v76, 0xffff0000, v68
	v_and_b32_e32 v77, 0xffff0000, v69
	v_mul_f32_e32 v196, s51, v76
	v_mul_f32_e32 v198, s64, v77
	v_cvt_scalef32_pk_f32_fp4 v[228:229], v36, 1.0
	v_cvt_scalef32_pk_f32_fp4 v[230:231], v36, 1.0 op_sel:[1,0,0]
	v_cvt_scalef32_pk_f32_fp4 v[232:233], v36, 1.0 op_sel:[0,1,0]
	v_cvt_scalef32_pk_f32_fp4 v[234:235], v36, 1.0 op_sel:[1,1,0]
	v_pk_fma_f32 v[178:179], v[196:197], v[228:229], v[178:179] op_sel_hi:[0,1,1]
	v_pk_fma_f32 v[184:185], v[196:197], v[230:231], v[184:185] op_sel_hi:[0,1,1]
	v_pk_fma_f32 v[182:183], v[196:197], v[232:233], v[182:183] op_sel_hi:[0,1,1]
	v_pk_fma_f32 v[180:181], v[196:197], v[234:235], v[180:181] op_sel_hi:[0,1,1]
	v_cvt_scalef32_pk_f32_fp4 v[236:237], v40, 1.0
	v_cvt_scalef32_pk_f32_fp4 v[238:239], v40, 1.0 op_sel:[1,0,0]
	v_cvt_scalef32_pk_f32_fp4 v[240:241], v40, 1.0 op_sel:[0,1,0]
	v_cvt_scalef32_pk_f32_fp4 v[242:243], v40, 1.0 op_sel:[1,1,0]
	v_pk_fma_f32 v[178:179], v[198:199], v[236:237], v[178:179] op_sel_hi:[0,1,1]
	v_pk_fma_f32 v[184:185], v[198:199], v[238:239], v[184:185] op_sel_hi:[0,1,1]
	v_pk_fma_f32 v[182:183], v[198:199], v[240:241], v[182:183] op_sel_hi:[0,1,1]
	v_pk_fma_f32 v[180:181], v[198:199], v[242:243], v[180:181] op_sel_hi:[0,1,1]
	v_cvt_scalef32_pk_f32_fp4 v[228:229], v37, 1.0
	v_cvt_scalef32_pk_f32_fp4 v[230:231], v37, 1.0 op_sel:[1,0,0]
	v_cvt_scalef32_pk_f32_fp4 v[232:233], v37, 1.0 op_sel:[0,1,0]
	v_cvt_scalef32_pk_f32_fp4 v[234:235], v37, 1.0 op_sel:[1,1,0]
	v_pk_fma_f32 v[176:177], v[196:197], v[228:229], v[176:177] op_sel_hi:[0,1,1]
	v_pk_fma_f32 v[174:175], v[196:197], v[230:231], v[174:175] op_sel_hi:[0,1,1]
	v_pk_fma_f32 v[160:161], v[196:197], v[232:233], v[160:161] op_sel_hi:[0,1,1]
	v_pk_fma_f32 v[158:159], v[196:197], v[234:235], v[158:159] op_sel_hi:[0,1,1]
	v_cvt_scalef32_pk_f32_fp4 v[236:237], v41, 1.0
	v_cvt_scalef32_pk_f32_fp4 v[238:239], v41, 1.0 op_sel:[1,0,0]
	v_cvt_scalef32_pk_f32_fp4 v[240:241], v41, 1.0 op_sel:[0,1,0]
	v_cvt_scalef32_pk_f32_fp4 v[242:243], v41, 1.0 op_sel:[1,1,0]
	v_pk_fma_f32 v[176:177], v[198:199], v[236:237], v[176:177] op_sel_hi:[0,1,1]
	v_pk_fma_f32 v[174:175], v[198:199], v[238:239], v[174:175] op_sel_hi:[0,1,1]
	v_pk_fma_f32 v[160:161], v[198:199], v[240:241], v[160:161] op_sel_hi:[0,1,1]
	v_pk_fma_f32 v[158:159], v[198:199], v[242:243], v[158:159] op_sel_hi:[0,1,1]
	v_cvt_scalef32_pk_f32_fp4 v[228:229], v38, 1.0
	v_cvt_scalef32_pk_f32_fp4 v[230:231], v38, 1.0 op_sel:[1,0,0]
	v_cvt_scalef32_pk_f32_fp4 v[232:233], v38, 1.0 op_sel:[0,1,0]
	v_cvt_scalef32_pk_f32_fp4 v[234:235], v38, 1.0 op_sel:[1,1,0]
	v_pk_fma_f32 v[156:157], v[196:197], v[228:229], v[156:157] op_sel_hi:[0,1,1]
	v_pk_fma_f32 v[154:155], v[196:197], v[230:231], v[154:155] op_sel_hi:[0,1,1]
	v_pk_fma_f32 v[152:153], v[196:197], v[232:233], v[152:153] op_sel_hi:[0,1,1]
	v_pk_fma_f32 v[150:151], v[196:197], v[234:235], v[150:151] op_sel_hi:[0,1,1]
	v_cvt_scalef32_pk_f32_fp4 v[236:237], v42, 1.0
	v_cvt_scalef32_pk_f32_fp4 v[238:239], v42, 1.0 op_sel:[1,0,0]
	v_cvt_scalef32_pk_f32_fp4 v[240:241], v42, 1.0 op_sel:[0,1,0]
	v_cvt_scalef32_pk_f32_fp4 v[242:243], v42, 1.0 op_sel:[1,1,0]
	v_pk_fma_f32 v[156:157], v[198:199], v[236:237], v[156:157] op_sel_hi:[0,1,1]
	v_pk_fma_f32 v[154:155], v[198:199], v[238:239], v[154:155] op_sel_hi:[0,1,1]
	v_pk_fma_f32 v[152:153], v[198:199], v[240:241], v[152:153] op_sel_hi:[0,1,1]
	v_pk_fma_f32 v[150:151], v[198:199], v[242:243], v[150:151] op_sel_hi:[0,1,1]
	v_cvt_scalef32_pk_f32_fp4 v[228:229], v39, 1.0
	v_cvt_scalef32_pk_f32_fp4 v[230:231], v39, 1.0 op_sel:[1,0,0]
	v_cvt_scalef32_pk_f32_fp4 v[232:233], v39, 1.0 op_sel:[0,1,0]
	v_cvt_scalef32_pk_f32_fp4 v[234:235], v39, 1.0 op_sel:[1,1,0]
	v_pk_fma_f32 v[148:149], v[196:197], v[228:229], v[148:149] op_sel_hi:[0,1,1]
	v_pk_fma_f32 v[146:147], v[196:197], v[230:231], v[146:147] op_sel_hi:[0,1,1]
	v_pk_fma_f32 v[144:145], v[196:197], v[232:233], v[144:145] op_sel_hi:[0,1,1]
	v_pk_fma_f32 v[142:143], v[196:197], v[234:235], v[142:143] op_sel_hi:[0,1,1]
	v_cvt_scalef32_pk_f32_fp4 v[236:237], v43, 1.0
	v_cvt_scalef32_pk_f32_fp4 v[238:239], v43, 1.0 op_sel:[1,0,0]
	v_cvt_scalef32_pk_f32_fp4 v[240:241], v43, 1.0 op_sel:[0,1,0]
	v_cvt_scalef32_pk_f32_fp4 v[242:243], v43, 1.0 op_sel:[1,1,0]
	v_pk_fma_f32 v[148:149], v[198:199], v[236:237], v[148:149] op_sel_hi:[0,1,1]
	v_pk_fma_f32 v[146:147], v[198:199], v[238:239], v[146:147] op_sel_hi:[0,1,1]
	v_pk_fma_f32 v[144:145], v[198:199], v[240:241], v[144:145] op_sel_hi:[0,1,1]
	v_pk_fma_f32 v[142:143], v[198:199], v[242:243], v[142:143] op_sel_hi:[0,1,1]
	s_add_u32 s0, s89, s24
	s_addc_u32 s1, s92, 0
	global_load_dwordx4 v[36:39], v81, s[0:1]
	s_add_u32 s4, s89, s28
	s_addc_u32 s5, s92, 0
	global_load_dwordx4 v[40:43], v81, s[4:5]
	s_lshr_b32 s8, s24, 6
	s_add_u32 s8, s6, s8
	s_addc_u32 s9, s88, 0
	global_load_dword v68, v83, s[8:9]
	s_lshr_b32 s14, s28, 6
	s_add_u32 s14, s6, s14
	s_addc_u32 s15, s88, 0
	global_load_dword v69, v83, s[14:15]
	s_waitcnt vmcnt(22)
	v_and_b32_e32 v76, 0xffff0000, v70
	v_and_b32_e32 v77, 0xffff0000, v71
	v_mul_f32_e32 v196, s65, v76
	v_mul_f32_e32 v198, s78, v77
	v_cvt_scalef32_pk_f32_fp4 v[228:229], v44, 1.0
	v_cvt_scalef32_pk_f32_fp4 v[230:231], v44, 1.0 op_sel:[1,0,0]
	v_cvt_scalef32_pk_f32_fp4 v[232:233], v44, 1.0 op_sel:[0,1,0]
	v_cvt_scalef32_pk_f32_fp4 v[234:235], v44, 1.0 op_sel:[1,1,0]
	v_pk_fma_f32 v[178:179], v[196:197], v[228:229], v[178:179] op_sel_hi:[0,1,1]
	v_pk_fma_f32 v[184:185], v[196:197], v[230:231], v[184:185] op_sel_hi:[0,1,1]
	v_pk_fma_f32 v[182:183], v[196:197], v[232:233], v[182:183] op_sel_hi:[0,1,1]
	v_pk_fma_f32 v[180:181], v[196:197], v[234:235], v[180:181] op_sel_hi:[0,1,1]
	v_cvt_scalef32_pk_f32_fp4 v[236:237], v48, 1.0
	v_cvt_scalef32_pk_f32_fp4 v[238:239], v48, 1.0 op_sel:[1,0,0]
	v_cvt_scalef32_pk_f32_fp4 v[240:241], v48, 1.0 op_sel:[0,1,0]
	v_cvt_scalef32_pk_f32_fp4 v[242:243], v48, 1.0 op_sel:[1,1,0]
	v_pk_fma_f32 v[178:179], v[198:199], v[236:237], v[178:179] op_sel_hi:[0,1,1]
	v_pk_fma_f32 v[184:185], v[198:199], v[238:239], v[184:185] op_sel_hi:[0,1,1]
	v_pk_fma_f32 v[182:183], v[198:199], v[240:241], v[182:183] op_sel_hi:[0,1,1]
	v_pk_fma_f32 v[180:181], v[198:199], v[242:243], v[180:181] op_sel_hi:[0,1,1]
	v_cvt_scalef32_pk_f32_fp4 v[228:229], v45, 1.0
	v_cvt_scalef32_pk_f32_fp4 v[230:231], v45, 1.0 op_sel:[1,0,0]
	v_cvt_scalef32_pk_f32_fp4 v[232:233], v45, 1.0 op_sel:[0,1,0]
	v_cvt_scalef32_pk_f32_fp4 v[234:235], v45, 1.0 op_sel:[1,1,0]
	v_pk_fma_f32 v[176:177], v[196:197], v[228:229], v[176:177] op_sel_hi:[0,1,1]
	v_pk_fma_f32 v[174:175], v[196:197], v[230:231], v[174:175] op_sel_hi:[0,1,1]
	v_pk_fma_f32 v[160:161], v[196:197], v[232:233], v[160:161] op_sel_hi:[0,1,1]
	v_pk_fma_f32 v[158:159], v[196:197], v[234:235], v[158:159] op_sel_hi:[0,1,1]
	v_cvt_scalef32_pk_f32_fp4 v[236:237], v49, 1.0
	v_cvt_scalef32_pk_f32_fp4 v[238:239], v49, 1.0 op_sel:[1,0,0]
	v_cvt_scalef32_pk_f32_fp4 v[240:241], v49, 1.0 op_sel:[0,1,0]
	v_cvt_scalef32_pk_f32_fp4 v[242:243], v49, 1.0 op_sel:[1,1,0]
	v_pk_fma_f32 v[176:177], v[198:199], v[236:237], v[176:177] op_sel_hi:[0,1,1]
	v_pk_fma_f32 v[174:175], v[198:199], v[238:239], v[174:175] op_sel_hi:[0,1,1]
	v_pk_fma_f32 v[160:161], v[198:199], v[240:241], v[160:161] op_sel_hi:[0,1,1]
	v_pk_fma_f32 v[158:159], v[198:199], v[242:243], v[158:159] op_sel_hi:[0,1,1]
	v_cvt_scalef32_pk_f32_fp4 v[228:229], v46, 1.0
	v_cvt_scalef32_pk_f32_fp4 v[230:231], v46, 1.0 op_sel:[1,0,0]
	v_cvt_scalef32_pk_f32_fp4 v[232:233], v46, 1.0 op_sel:[0,1,0]
	v_cvt_scalef32_pk_f32_fp4 v[234:235], v46, 1.0 op_sel:[1,1,0]
	v_pk_fma_f32 v[156:157], v[196:197], v[228:229], v[156:157] op_sel_hi:[0,1,1]
	v_pk_fma_f32 v[154:155], v[196:197], v[230:231], v[154:155] op_sel_hi:[0,1,1]
	v_pk_fma_f32 v[152:153], v[196:197], v[232:233], v[152:153] op_sel_hi:[0,1,1]
	v_pk_fma_f32 v[150:151], v[196:197], v[234:235], v[150:151] op_sel_hi:[0,1,1]
	v_cvt_scalef32_pk_f32_fp4 v[236:237], v50, 1.0
	v_cvt_scalef32_pk_f32_fp4 v[238:239], v50, 1.0 op_sel:[1,0,0]
	v_cvt_scalef32_pk_f32_fp4 v[240:241], v50, 1.0 op_sel:[0,1,0]
	v_cvt_scalef32_pk_f32_fp4 v[242:243], v50, 1.0 op_sel:[1,1,0]
	v_pk_fma_f32 v[156:157], v[198:199], v[236:237], v[156:157] op_sel_hi:[0,1,1]
	v_pk_fma_f32 v[154:155], v[198:199], v[238:239], v[154:155] op_sel_hi:[0,1,1]
	v_pk_fma_f32 v[152:153], v[198:199], v[240:241], v[152:153] op_sel_hi:[0,1,1]
	v_pk_fma_f32 v[150:151], v[198:199], v[242:243], v[150:151] op_sel_hi:[0,1,1]
	v_cvt_scalef32_pk_f32_fp4 v[228:229], v47, 1.0
	v_cvt_scalef32_pk_f32_fp4 v[230:231], v47, 1.0 op_sel:[1,0,0]
	v_cvt_scalef32_pk_f32_fp4 v[232:233], v47, 1.0 op_sel:[0,1,0]
	v_cvt_scalef32_pk_f32_fp4 v[234:235], v47, 1.0 op_sel:[1,1,0]
	v_pk_fma_f32 v[148:149], v[196:197], v[228:229], v[148:149] op_sel_hi:[0,1,1]
	v_pk_fma_f32 v[146:147], v[196:197], v[230:231], v[146:147] op_sel_hi:[0,1,1]
	v_pk_fma_f32 v[144:145], v[196:197], v[232:233], v[144:145] op_sel_hi:[0,1,1]
	v_pk_fma_f32 v[142:143], v[196:197], v[234:235], v[142:143] op_sel_hi:[0,1,1]
	v_cvt_scalef32_pk_f32_fp4 v[236:237], v51, 1.0
	v_cvt_scalef32_pk_f32_fp4 v[238:239], v51, 1.0 op_sel:[1,0,0]
	v_cvt_scalef32_pk_f32_fp4 v[240:241], v51, 1.0 op_sel:[0,1,0]
	v_cvt_scalef32_pk_f32_fp4 v[242:243], v51, 1.0 op_sel:[1,1,0]
	v_pk_fma_f32 v[148:149], v[198:199], v[236:237], v[148:149] op_sel_hi:[0,1,1]
	v_pk_fma_f32 v[146:147], v[198:199], v[238:239], v[146:147] op_sel_hi:[0,1,1]
	v_pk_fma_f32 v[144:145], v[198:199], v[240:241], v[144:145] op_sel_hi:[0,1,1]
	v_pk_fma_f32 v[142:143], v[198:199], v[242:243], v[142:143] op_sel_hi:[0,1,1]
	s_add_u32 s0, s89, s29
	s_addc_u32 s1, s92, 0
	global_load_dwordx4 v[44:47], v81, s[0:1]
	s_add_u32 s4, s89, s34
	s_addc_u32 s5, s92, 0
	global_load_dwordx4 v[48:51], v81, s[4:5]
	s_lshr_b32 s8, s29, 6
	s_add_u32 s8, s6, s8
	s_addc_u32 s9, s88, 0
	global_load_dword v70, v83, s[8:9]
	s_lshr_b32 s14, s34, 6
	s_add_u32 s14, s6, s14
	s_addc_u32 s15, s88, 0
	global_load_dword v71, v83, s[14:15]
	s_waitcnt vmcnt(22)
	v_and_b32_e32 v76, 0xffff0000, v72
	v_and_b32_e32 v77, 0xffff0000, v73
	v_mul_f32_e32 v196, s79, v76
	v_mul_f32_e32 v198, s82, v77
	v_cvt_scalef32_pk_f32_fp4 v[228:229], v52, 1.0
	v_cvt_scalef32_pk_f32_fp4 v[230:231], v52, 1.0 op_sel:[1,0,0]
	v_cvt_scalef32_pk_f32_fp4 v[232:233], v52, 1.0 op_sel:[0,1,0]
	v_cvt_scalef32_pk_f32_fp4 v[234:235], v52, 1.0 op_sel:[1,1,0]
	v_pk_fma_f32 v[178:179], v[196:197], v[228:229], v[178:179] op_sel_hi:[0,1,1]
	v_pk_fma_f32 v[184:185], v[196:197], v[230:231], v[184:185] op_sel_hi:[0,1,1]
	v_pk_fma_f32 v[182:183], v[196:197], v[232:233], v[182:183] op_sel_hi:[0,1,1]
	v_pk_fma_f32 v[180:181], v[196:197], v[234:235], v[180:181] op_sel_hi:[0,1,1]
	v_cvt_scalef32_pk_f32_fp4 v[236:237], v56, 1.0
	v_cvt_scalef32_pk_f32_fp4 v[238:239], v56, 1.0 op_sel:[1,0,0]
	v_cvt_scalef32_pk_f32_fp4 v[240:241], v56, 1.0 op_sel:[0,1,0]
	v_cvt_scalef32_pk_f32_fp4 v[242:243], v56, 1.0 op_sel:[1,1,0]
	v_pk_fma_f32 v[178:179], v[198:199], v[236:237], v[178:179] op_sel_hi:[0,1,1]
	v_pk_fma_f32 v[184:185], v[198:199], v[238:239], v[184:185] op_sel_hi:[0,1,1]
	v_pk_fma_f32 v[182:183], v[198:199], v[240:241], v[182:183] op_sel_hi:[0,1,1]
	v_pk_fma_f32 v[180:181], v[198:199], v[242:243], v[180:181] op_sel_hi:[0,1,1]
	v_cvt_scalef32_pk_f32_fp4 v[228:229], v53, 1.0
	v_cvt_scalef32_pk_f32_fp4 v[230:231], v53, 1.0 op_sel:[1,0,0]
	v_cvt_scalef32_pk_f32_fp4 v[232:233], v53, 1.0 op_sel:[0,1,0]
	v_cvt_scalef32_pk_f32_fp4 v[234:235], v53, 1.0 op_sel:[1,1,0]
	v_pk_fma_f32 v[176:177], v[196:197], v[228:229], v[176:177] op_sel_hi:[0,1,1]
	v_pk_fma_f32 v[174:175], v[196:197], v[230:231], v[174:175] op_sel_hi:[0,1,1]
	v_pk_fma_f32 v[160:161], v[196:197], v[232:233], v[160:161] op_sel_hi:[0,1,1]
	v_pk_fma_f32 v[158:159], v[196:197], v[234:235], v[158:159] op_sel_hi:[0,1,1]
	v_cvt_scalef32_pk_f32_fp4 v[236:237], v57, 1.0
	v_cvt_scalef32_pk_f32_fp4 v[238:239], v57, 1.0 op_sel:[1,0,0]
	v_cvt_scalef32_pk_f32_fp4 v[240:241], v57, 1.0 op_sel:[0,1,0]
	v_cvt_scalef32_pk_f32_fp4 v[242:243], v57, 1.0 op_sel:[1,1,0]
	v_pk_fma_f32 v[176:177], v[198:199], v[236:237], v[176:177] op_sel_hi:[0,1,1]
	v_pk_fma_f32 v[174:175], v[198:199], v[238:239], v[174:175] op_sel_hi:[0,1,1]
	v_pk_fma_f32 v[160:161], v[198:199], v[240:241], v[160:161] op_sel_hi:[0,1,1]
	v_pk_fma_f32 v[158:159], v[198:199], v[242:243], v[158:159] op_sel_hi:[0,1,1]
	v_cvt_scalef32_pk_f32_fp4 v[228:229], v54, 1.0
	v_cvt_scalef32_pk_f32_fp4 v[230:231], v54, 1.0 op_sel:[1,0,0]
	v_cvt_scalef32_pk_f32_fp4 v[232:233], v54, 1.0 op_sel:[0,1,0]
	v_cvt_scalef32_pk_f32_fp4 v[234:235], v54, 1.0 op_sel:[1,1,0]
	v_pk_fma_f32 v[156:157], v[196:197], v[228:229], v[156:157] op_sel_hi:[0,1,1]
	v_pk_fma_f32 v[154:155], v[196:197], v[230:231], v[154:155] op_sel_hi:[0,1,1]
	v_pk_fma_f32 v[152:153], v[196:197], v[232:233], v[152:153] op_sel_hi:[0,1,1]
	v_pk_fma_f32 v[150:151], v[196:197], v[234:235], v[150:151] op_sel_hi:[0,1,1]
	v_cvt_scalef32_pk_f32_fp4 v[236:237], v58, 1.0
	v_cvt_scalef32_pk_f32_fp4 v[238:239], v58, 1.0 op_sel:[1,0,0]
	v_cvt_scalef32_pk_f32_fp4 v[240:241], v58, 1.0 op_sel:[0,1,0]
	v_cvt_scalef32_pk_f32_fp4 v[242:243], v58, 1.0 op_sel:[1,1,0]
	v_pk_fma_f32 v[156:157], v[198:199], v[236:237], v[156:157] op_sel_hi:[0,1,1]
	v_pk_fma_f32 v[154:155], v[198:199], v[238:239], v[154:155] op_sel_hi:[0,1,1]
	v_pk_fma_f32 v[152:153], v[198:199], v[240:241], v[152:153] op_sel_hi:[0,1,1]
	v_pk_fma_f32 v[150:151], v[198:199], v[242:243], v[150:151] op_sel_hi:[0,1,1]
	v_cvt_scalef32_pk_f32_fp4 v[228:229], v55, 1.0
	v_cvt_scalef32_pk_f32_fp4 v[230:231], v55, 1.0 op_sel:[1,0,0]
	v_cvt_scalef32_pk_f32_fp4 v[232:233], v55, 1.0 op_sel:[0,1,0]
	v_cvt_scalef32_pk_f32_fp4 v[234:235], v55, 1.0 op_sel:[1,1,0]
	v_pk_fma_f32 v[148:149], v[196:197], v[228:229], v[148:149] op_sel_hi:[0,1,1]
	v_pk_fma_f32 v[146:147], v[196:197], v[230:231], v[146:147] op_sel_hi:[0,1,1]
	v_pk_fma_f32 v[144:145], v[196:197], v[232:233], v[144:145] op_sel_hi:[0,1,1]
	v_pk_fma_f32 v[142:143], v[196:197], v[234:235], v[142:143] op_sel_hi:[0,1,1]
	v_cvt_scalef32_pk_f32_fp4 v[236:237], v59, 1.0
	v_cvt_scalef32_pk_f32_fp4 v[238:239], v59, 1.0 op_sel:[1,0,0]
	v_cvt_scalef32_pk_f32_fp4 v[240:241], v59, 1.0 op_sel:[0,1,0]
	v_cvt_scalef32_pk_f32_fp4 v[242:243], v59, 1.0 op_sel:[1,1,0]
	v_pk_fma_f32 v[148:149], v[198:199], v[236:237], v[148:149] op_sel_hi:[0,1,1]
	v_pk_fma_f32 v[146:147], v[198:199], v[238:239], v[146:147] op_sel_hi:[0,1,1]
	v_pk_fma_f32 v[144:145], v[198:199], v[240:241], v[144:145] op_sel_hi:[0,1,1]
	v_pk_fma_f32 v[142:143], v[198:199], v[242:243], v[142:143] op_sel_hi:[0,1,1]
	s_add_u32 s0, s89, s35
	s_addc_u32 s1, s92, 0
	global_load_dwordx4 v[52:55], v81, s[0:1]
	s_add_u32 s4, s89, s42
	s_addc_u32 s5, s92, 0
	global_load_dwordx4 v[56:59], v81, s[4:5]
	s_lshr_b32 s8, s35, 6
	s_add_u32 s8, s6, s8
	s_addc_u32 s9, s88, 0
	global_load_dword v72, v83, s[8:9]
	s_lshr_b32 s14, s42, 6
	s_add_u32 s14, s6, s14
	s_addc_u32 s15, s88, 0
	global_load_dword v73, v83, s[14:15]
	s_waitcnt vmcnt(22)
	v_and_b32_e32 v76, 0xffff0000, v74
	v_and_b32_e32 v77, 0xffff0000, v75
	v_mul_f32_e32 v196, s84, v76
	v_mul_f32_e32 v198, s10, v77
	v_cvt_scalef32_pk_f32_fp4 v[228:229], v60, 1.0
	v_cvt_scalef32_pk_f32_fp4 v[230:231], v60, 1.0 op_sel:[1,0,0]
	v_cvt_scalef32_pk_f32_fp4 v[232:233], v60, 1.0 op_sel:[0,1,0]
	v_cvt_scalef32_pk_f32_fp4 v[234:235], v60, 1.0 op_sel:[1,1,0]
	v_pk_fma_f32 v[178:179], v[196:197], v[228:229], v[178:179] op_sel_hi:[0,1,1]
	v_pk_fma_f32 v[184:185], v[196:197], v[230:231], v[184:185] op_sel_hi:[0,1,1]
	v_pk_fma_f32 v[182:183], v[196:197], v[232:233], v[182:183] op_sel_hi:[0,1,1]
	v_pk_fma_f32 v[180:181], v[196:197], v[234:235], v[180:181] op_sel_hi:[0,1,1]
	v_cvt_scalef32_pk_f32_fp4 v[236:237], v64, 1.0
	v_cvt_scalef32_pk_f32_fp4 v[238:239], v64, 1.0 op_sel:[1,0,0]
	v_cvt_scalef32_pk_f32_fp4 v[240:241], v64, 1.0 op_sel:[0,1,0]
	v_cvt_scalef32_pk_f32_fp4 v[242:243], v64, 1.0 op_sel:[1,1,0]
	v_pk_fma_f32 v[178:179], v[198:199], v[236:237], v[178:179] op_sel_hi:[0,1,1]
	v_pk_fma_f32 v[184:185], v[198:199], v[238:239], v[184:185] op_sel_hi:[0,1,1]
	v_pk_fma_f32 v[182:183], v[198:199], v[240:241], v[182:183] op_sel_hi:[0,1,1]
	v_pk_fma_f32 v[180:181], v[198:199], v[242:243], v[180:181] op_sel_hi:[0,1,1]
	v_cvt_scalef32_pk_f32_fp4 v[228:229], v61, 1.0
	v_cvt_scalef32_pk_f32_fp4 v[230:231], v61, 1.0 op_sel:[1,0,0]
	v_cvt_scalef32_pk_f32_fp4 v[232:233], v61, 1.0 op_sel:[0,1,0]
	v_cvt_scalef32_pk_f32_fp4 v[234:235], v61, 1.0 op_sel:[1,1,0]
	v_pk_fma_f32 v[176:177], v[196:197], v[228:229], v[176:177] op_sel_hi:[0,1,1]
	v_pk_fma_f32 v[174:175], v[196:197], v[230:231], v[174:175] op_sel_hi:[0,1,1]
	v_pk_fma_f32 v[160:161], v[196:197], v[232:233], v[160:161] op_sel_hi:[0,1,1]
	v_pk_fma_f32 v[158:159], v[196:197], v[234:235], v[158:159] op_sel_hi:[0,1,1]
	v_cvt_scalef32_pk_f32_fp4 v[236:237], v65, 1.0
	v_cvt_scalef32_pk_f32_fp4 v[238:239], v65, 1.0 op_sel:[1,0,0]
	v_cvt_scalef32_pk_f32_fp4 v[240:241], v65, 1.0 op_sel:[0,1,0]
	v_cvt_scalef32_pk_f32_fp4 v[242:243], v65, 1.0 op_sel:[1,1,0]
	v_pk_fma_f32 v[176:177], v[198:199], v[236:237], v[176:177] op_sel_hi:[0,1,1]
	v_pk_fma_f32 v[174:175], v[198:199], v[238:239], v[174:175] op_sel_hi:[0,1,1]
	v_pk_fma_f32 v[160:161], v[198:199], v[240:241], v[160:161] op_sel_hi:[0,1,1]
	v_pk_fma_f32 v[158:159], v[198:199], v[242:243], v[158:159] op_sel_hi:[0,1,1]
	v_cvt_scalef32_pk_f32_fp4 v[228:229], v62, 1.0
	v_cvt_scalef32_pk_f32_fp4 v[230:231], v62, 1.0 op_sel:[1,0,0]
	v_cvt_scalef32_pk_f32_fp4 v[232:233], v62, 1.0 op_sel:[0,1,0]
	v_cvt_scalef32_pk_f32_fp4 v[234:235], v62, 1.0 op_sel:[1,1,0]
	v_pk_fma_f32 v[156:157], v[196:197], v[228:229], v[156:157] op_sel_hi:[0,1,1]
	v_pk_fma_f32 v[154:155], v[196:197], v[230:231], v[154:155] op_sel_hi:[0,1,1]
	v_pk_fma_f32 v[152:153], v[196:197], v[232:233], v[152:153] op_sel_hi:[0,1,1]
	v_pk_fma_f32 v[150:151], v[196:197], v[234:235], v[150:151] op_sel_hi:[0,1,1]
	v_cvt_scalef32_pk_f32_fp4 v[236:237], v66, 1.0
	v_cvt_scalef32_pk_f32_fp4 v[238:239], v66, 1.0 op_sel:[1,0,0]
	v_cvt_scalef32_pk_f32_fp4 v[240:241], v66, 1.0 op_sel:[0,1,0]
	v_cvt_scalef32_pk_f32_fp4 v[242:243], v66, 1.0 op_sel:[1,1,0]
	v_pk_fma_f32 v[156:157], v[198:199], v[236:237], v[156:157] op_sel_hi:[0,1,1]
	v_pk_fma_f32 v[154:155], v[198:199], v[238:239], v[154:155] op_sel_hi:[0,1,1]
	v_pk_fma_f32 v[152:153], v[198:199], v[240:241], v[152:153] op_sel_hi:[0,1,1]
	v_pk_fma_f32 v[150:151], v[198:199], v[242:243], v[150:151] op_sel_hi:[0,1,1]
	v_cvt_scalef32_pk_f32_fp4 v[228:229], v63, 1.0
	v_cvt_scalef32_pk_f32_fp4 v[230:231], v63, 1.0 op_sel:[1,0,0]
	v_cvt_scalef32_pk_f32_fp4 v[232:233], v63, 1.0 op_sel:[0,1,0]
	v_cvt_scalef32_pk_f32_fp4 v[234:235], v63, 1.0 op_sel:[1,1,0]
	v_pk_fma_f32 v[148:149], v[196:197], v[228:229], v[148:149] op_sel_hi:[0,1,1]
	v_pk_fma_f32 v[146:147], v[196:197], v[230:231], v[146:147] op_sel_hi:[0,1,1]
	v_pk_fma_f32 v[144:145], v[196:197], v[232:233], v[144:145] op_sel_hi:[0,1,1]
	v_pk_fma_f32 v[142:143], v[196:197], v[234:235], v[142:143] op_sel_hi:[0,1,1]
	v_cvt_scalef32_pk_f32_fp4 v[236:237], v67, 1.0
	v_cvt_scalef32_pk_f32_fp4 v[238:239], v67, 1.0 op_sel:[1,0,0]
	v_cvt_scalef32_pk_f32_fp4 v[240:241], v67, 1.0 op_sel:[0,1,0]
	v_cvt_scalef32_pk_f32_fp4 v[242:243], v67, 1.0 op_sel:[1,1,0]
	v_pk_fma_f32 v[148:149], v[198:199], v[236:237], v[148:149] op_sel_hi:[0,1,1]
	v_pk_fma_f32 v[146:147], v[198:199], v[238:239], v[146:147] op_sel_hi:[0,1,1]
	v_pk_fma_f32 v[144:145], v[198:199], v[240:241], v[144:145] op_sel_hi:[0,1,1]
	v_pk_fma_f32 v[142:143], v[198:199], v[242:243], v[142:143] op_sel_hi:[0,1,1]
	s_add_u32 s0, s89, s43
	s_addc_u32 s1, s92, 0
	global_load_dwordx4 v[60:63], v81, s[0:1]
	s_add_u32 s4, s89, s50
	s_addc_u32 s5, s92, 0
	global_load_dwordx4 v[64:67], v81, s[4:5]
	s_lshr_b32 s8, s43, 6
	s_add_u32 s8, s6, s8
	s_addc_u32 s9, s88, 0
	global_load_dword v74, v83, s[8:9]
	s_lshr_b32 s14, s50, 6
	s_add_u32 s14, s6, s14
	s_addc_u32 s15, s88, 0
	global_load_dword v75, v83, s[14:15]
	s_add_i32 s2, s2, 64
	s_cmpk_lt_u32 s2, 0x3c0
	s_cbranch_scc1 .Lgm_loop
	v_add_u32_e32 v251, s2, v213
	ds_read_b32 v201, v251
	s_waitcnt vmcnt(22)
	v_cvt_scalef32_pk_f32_fp4 v[228:229], v0, 1.0
	v_cvt_scalef32_pk_f32_fp4 v[230:231], v0, 1.0 op_sel:[1,0,0]
	v_cvt_scalef32_pk_f32_fp4 v[232:233], v0, 1.0 op_sel:[0,1,0]
	v_cvt_scalef32_pk_f32_fp4 v[234:235], v0, 1.0 op_sel:[1,1,0]
	v_cvt_scalef32_pk_f32_fp4 v[236:237], v4, 1.0
	v_cvt_scalef32_pk_f32_fp4 v[238:239], v4, 1.0 op_sel:[1,0,0]
	v_cvt_scalef32_pk_f32_fp4 v[240:241], v4, 1.0 op_sel:[0,1,0]
	v_cvt_scalef32_pk_f32_fp4 v[242:243], v4, 1.0 op_sel:[1,1,0]
	v_pk_mul_f32 v[244:245], v[228:229], v[102:103]
	v_pk_mul_f32 v[246:247], v[236:237], v[102:103]
	v_pk_fma_f32 v[244:245], v[230:231], v[104:105], v[244:245]
	v_pk_fma_f32 v[246:247], v[238:239], v[104:105], v[246:247]
	v_pk_fma_f32 v[244:245], v[232:233], v[106:107], v[244:245]
	v_pk_fma_f32 v[246:247], v[240:241], v[106:107], v[246:247]
	v_pk_fma_f32 v[244:245], v[234:235], v[108:109], v[244:245]
	v_pk_fma_f32 v[246:247], v[242:243], v[108:109], v[246:247]
	v_cvt_scalef32_pk_f32_fp4 v[228:229], v1, 1.0
	v_cvt_scalef32_pk_f32_fp4 v[230:231], v1, 1.0 op_sel:[1,0,0]
	v_cvt_scalef32_pk_f32_fp4 v[232:233], v1, 1.0 op_sel:[0,1,0]
	v_cvt_scalef32_pk_f32_fp4 v[234:235], v1, 1.0 op_sel:[1,1,0]
	v_cvt_scalef32_pk_f32_fp4 v[236:237], v5, 1.0
	v_cvt_scalef32_pk_f32_fp4 v[238:239], v5, 1.0 op_sel:[1,0,0]
	v_cvt_scalef32_pk_f32_fp4 v[240:241], v5, 1.0 op_sel:[0,1,0]
	v_cvt_scalef32_pk_f32_fp4 v[242:243], v5, 1.0 op_sel:[1,1,0]
	v_pk_fma_f32 v[244:245], v[228:229], v[110:111], v[244:245]
	v_pk_fma_f32 v[246:247], v[236:237], v[110:111], v[246:247]
	v_pk_fma_f32 v[244:245], v[230:231], v[112:113], v[244:245]
	v_pk_fma_f32 v[246:247], v[238:239], v[112:113], v[246:247]
	v_pk_fma_f32 v[244:245], v[232:233], v[114:115], v[244:245]
	v_pk_fma_f32 v[246:247], v[240:241], v[114:115], v[246:247]
	v_pk_fma_f32 v[244:245], v[234:235], v[116:117], v[244:245]
	v_pk_fma_f32 v[246:247], v[242:243], v[116:117], v[246:247]
	v_cvt_scalef32_pk_f32_fp4 v[228:229], v2, 1.0
	v_cvt_scalef32_pk_f32_fp4 v[230:231], v2, 1.0 op_sel:[1,0,0]
	v_cvt_scalef32_pk_f32_fp4 v[232:233], v2, 1.0 op_sel:[0,1,0]
	v_cvt_scalef32_pk_f32_fp4 v[234:235], v2, 1.0 op_sel:[1,1,0]
	v_cvt_scalef32_pk_f32_fp4 v[236:237], v6, 1.0
	v_cvt_scalef32_pk_f32_fp4 v[238:239], v6, 1.0 op_sel:[1,0,0]
	v_cvt_scalef32_pk_f32_fp4 v[240:241], v6, 1.0 op_sel:[0,1,0]
	v_cvt_scalef32_pk_f32_fp4 v[242:243], v6, 1.0 op_sel:[1,1,0]
	v_pk_fma_f32 v[244:245], v[228:229], v[118:119], v[244:245]
	v_pk_fma_f32 v[246:247], v[236:237], v[118:119], v[246:247]
	v_pk_fma_f32 v[244:245], v[230:231], v[120:121], v[244:245]
	v_pk_fma_f32 v[246:247], v[238:239], v[120:121], v[246:247]
	v_pk_fma_f32 v[244:245], v[232:233], v[122:123], v[244:245]
	v_pk_fma_f32 v[246:247], v[240:241], v[122:123], v[246:247]
	v_pk_fma_f32 v[244:245], v[234:235], v[124:125], v[244:245]
	v_pk_fma_f32 v[246:247], v[242:243], v[124:125], v[246:247]
	v_cvt_scalef32_pk_f32_fp4 v[228:229], v3, 1.0
	v_cvt_scalef32_pk_f32_fp4 v[230:231], v3, 1.0 op_sel:[1,0,0]
	v_cvt_scalef32_pk_f32_fp4 v[232:233], v3, 1.0 op_sel:[0,1,0]
	v_cvt_scalef32_pk_f32_fp4 v[234:235], v3, 1.0 op_sel:[1,1,0]
	v_cvt_scalef32_pk_f32_fp4 v[236:237], v7, 1.0
	v_cvt_scalef32_pk_f32_fp4 v[238:239], v7, 1.0 op_sel:[1,0,0]
	v_cvt_scalef32_pk_f32_fp4 v[240:241], v7, 1.0 op_sel:[0,1,0]
	v_cvt_scalef32_pk_f32_fp4 v[242:243], v7, 1.0 op_sel:[1,1,0]
	v_pk_fma_f32 v[244:245], v[228:229], v[126:127], v[244:245]
	v_pk_fma_f32 v[246:247], v[236:237], v[126:127], v[246:247]
	v_pk_fma_f32 v[244:245], v[230:231], v[128:129], v[244:245]
	v_pk_fma_f32 v[246:247], v[238:239], v[128:129], v[246:247]
	v_pk_fma_f32 v[244:245], v[232:233], v[130:131], v[244:245]
	v_pk_fma_f32 v[246:247], v[240:241], v[130:131], v[246:247]
	v_pk_fma_f32 v[244:245], v[234:235], v[132:133], v[244:245]
	v_pk_fma_f32 v[246:247], v[242:243], v[132:133], v[246:247]
	v_add_f32_e32 v186, v244, v245
	v_add_f32_e32 v187, v246, v247
	s_waitcnt vmcnt(20)
	v_cvt_scalef32_pk_f32_fp4 v[228:229], v8, 1.0
	v_cvt_scalef32_pk_f32_fp4 v[230:231], v8, 1.0 op_sel:[1,0,0]
	v_cvt_scalef32_pk_f32_fp4 v[232:233], v8, 1.0 op_sel:[0,1,0]
	v_cvt_scalef32_pk_f32_fp4 v[234:235], v8, 1.0 op_sel:[1,1,0]
	v_cvt_scalef32_pk_f32_fp4 v[236:237], v12, 1.0
	v_cvt_scalef32_pk_f32_fp4 v[238:239], v12, 1.0 op_sel:[1,0,0]
	v_cvt_scalef32_pk_f32_fp4 v[240:241], v12, 1.0 op_sel:[0,1,0]
	v_cvt_scalef32_pk_f32_fp4 v[242:243], v12, 1.0 op_sel:[1,1,0]
	v_pk_mul_f32 v[244:245], v[228:229], v[102:103]
	v_pk_mul_f32 v[246:247], v[236:237], v[102:103]
	v_pk_fma_f32 v[244:245], v[230:231], v[104:105], v[244:245]
	v_pk_fma_f32 v[246:247], v[238:239], v[104:105], v[246:247]
	v_pk_fma_f32 v[244:245], v[232:233], v[106:107], v[244:245]
	v_pk_fma_f32 v[246:247], v[240:241], v[106:107], v[246:247]
	v_pk_fma_f32 v[244:245], v[234:235], v[108:109], v[244:245]
	v_pk_fma_f32 v[246:247], v[242:243], v[108:109], v[246:247]
	v_cvt_scalef32_pk_f32_fp4 v[228:229], v9, 1.0
	v_cvt_scalef32_pk_f32_fp4 v[230:231], v9, 1.0 op_sel:[1,0,0]
	v_cvt_scalef32_pk_f32_fp4 v[232:233], v9, 1.0 op_sel:[0,1,0]
	v_cvt_scalef32_pk_f32_fp4 v[234:235], v9, 1.0 op_sel:[1,1,0]
	v_cvt_scalef32_pk_f32_fp4 v[236:237], v13, 1.0
	v_cvt_scalef32_pk_f32_fp4 v[238:239], v13, 1.0 op_sel:[1,0,0]
	v_cvt_scalef32_pk_f32_fp4 v[240:241], v13, 1.0 op_sel:[0,1,0]
	v_cvt_scalef32_pk_f32_fp4 v[242:243], v13, 1.0 op_sel:[1,1,0]
	v_pk_fma_f32 v[244:245], v[228:229], v[110:111], v[244:245]
	v_pk_fma_f32 v[246:247], v[236:237], v[110:111], v[246:247]
	v_pk_fma_f32 v[244:245], v[230:231], v[112:113], v[244:245]
	v_pk_fma_f32 v[246:247], v[238:239], v[112:113], v[246:247]
	v_pk_fma_f32 v[244:245], v[232:233], v[114:115], v[244:245]
	v_pk_fma_f32 v[246:247], v[240:241], v[114:115], v[246:247]
	v_pk_fma_f32 v[244:245], v[234:235], v[116:117], v[244:245]
	v_pk_fma_f32 v[246:247], v[242:243], v[116:117], v[246:247]
	v_cvt_scalef32_pk_f32_fp4 v[228:229], v10, 1.0
	v_cvt_scalef32_pk_f32_fp4 v[230:231], v10, 1.0 op_sel:[1,0,0]
	v_cvt_scalef32_pk_f32_fp4 v[232:233], v10, 1.0 op_sel:[0,1,0]
	v_cvt_scalef32_pk_f32_fp4 v[234:235], v10, 1.0 op_sel:[1,1,0]
	v_cvt_scalef32_pk_f32_fp4 v[236:237], v14, 1.0
	v_cvt_scalef32_pk_f32_fp4 v[238:239], v14, 1.0 op_sel:[1,0,0]
	v_cvt_scalef32_pk_f32_fp4 v[240:241], v14, 1.0 op_sel:[0,1,0]
	v_cvt_scalef32_pk_f32_fp4 v[242:243], v14, 1.0 op_sel:[1,1,0]
	v_pk_fma_f32 v[244:245], v[228:229], v[118:119], v[244:245]
	v_pk_fma_f32 v[246:247], v[236:237], v[118:119], v[246:247]
	v_pk_fma_f32 v[244:245], v[230:231], v[120:121], v[244:245]
	v_pk_fma_f32 v[246:247], v[238:239], v[120:121], v[246:247]
	v_pk_fma_f32 v[244:245], v[232:233], v[122:123], v[244:245]
	v_pk_fma_f32 v[246:247], v[240:241], v[122:123], v[246:247]
	v_pk_fma_f32 v[244:245], v[234:235], v[124:125], v[244:245]
	v_pk_fma_f32 v[246:247], v[242:243], v[124:125], v[246:247]
	v_cvt_scalef32_pk_f32_fp4 v[228:229], v11, 1.0
	v_cvt_scalef32_pk_f32_fp4 v[230:231], v11, 1.0 op_sel:[1,0,0]
	v_cvt_scalef32_pk_f32_fp4 v[232:233], v11, 1.0 op_sel:[0,1,0]
	v_cvt_scalef32_pk_f32_fp4 v[234:235], v11, 1.0 op_sel:[1,1,0]
	v_cvt_scalef32_pk_f32_fp4 v[236:237], v15, 1.0
	v_cvt_scalef32_pk_f32_fp4 v[238:239], v15, 1.0 op_sel:[1,0,0]
	v_cvt_scalef32_pk_f32_fp4 v[240:241], v15, 1.0 op_sel:[0,1,0]
	v_cvt_scalef32_pk_f32_fp4 v[242:243], v15, 1.0 op_sel:[1,1,0]
	v_pk_fma_f32 v[244:245], v[228:229], v[126:127], v[244:245]
	v_pk_fma_f32 v[246:247], v[236:237], v[126:127], v[246:247]
	v_pk_fma_f32 v[244:245], v[230:231], v[128:129], v[244:245]
	v_pk_fma_f32 v[246:247], v[238:239], v[128:129], v[246:247]
	v_pk_fma_f32 v[244:245], v[232:233], v[130:131], v[244:245]
	v_pk_fma_f32 v[246:247], v[240:241], v[130:131], v[246:247]
	v_pk_fma_f32 v[244:245], v[234:235], v[132:133], v[244:245]
	v_pk_fma_f32 v[246:247], v[242:243], v[132:133], v[246:247]
	v_add_f32_e32 v188, v244, v245
	v_add_f32_e32 v189, v246, v247
	s_waitcnt vmcnt(18)
	v_cvt_scalef32_pk_f32_fp4 v[228:229], v16, 1.0
	v_cvt_scalef32_pk_f32_fp4 v[230:231], v16, 1.0 op_sel:[1,0,0]
	v_cvt_scalef32_pk_f32_fp4 v[232:233], v16, 1.0 op_sel:[0,1,0]
	v_cvt_scalef32_pk_f32_fp4 v[234:235], v16, 1.0 op_sel:[1,1,0]
	v_cvt_scalef32_pk_f32_fp4 v[236:237], v20, 1.0
	v_cvt_scalef32_pk_f32_fp4 v[238:239], v20, 1.0 op_sel:[1,0,0]
	v_cvt_scalef32_pk_f32_fp4 v[240:241], v20, 1.0 op_sel:[0,1,0]
	v_cvt_scalef32_pk_f32_fp4 v[242:243], v20, 1.0 op_sel:[1,1,0]
	v_pk_mul_f32 v[244:245], v[228:229], v[102:103]
	v_pk_mul_f32 v[246:247], v[236:237], v[102:103]
	v_pk_fma_f32 v[244:245], v[230:231], v[104:105], v[244:245]
	v_pk_fma_f32 v[246:247], v[238:239], v[104:105], v[246:247]
	v_pk_fma_f32 v[244:245], v[232:233], v[106:107], v[244:245]
	v_pk_fma_f32 v[246:247], v[240:241], v[106:107], v[246:247]
	v_pk_fma_f32 v[244:245], v[234:235], v[108:109], v[244:245]
	v_pk_fma_f32 v[246:247], v[242:243], v[108:109], v[246:247]
	v_cvt_scalef32_pk_f32_fp4 v[228:229], v17, 1.0
	v_cvt_scalef32_pk_f32_fp4 v[230:231], v17, 1.0 op_sel:[1,0,0]
	v_cvt_scalef32_pk_f32_fp4 v[232:233], v17, 1.0 op_sel:[0,1,0]
	v_cvt_scalef32_pk_f32_fp4 v[234:235], v17, 1.0 op_sel:[1,1,0]
	v_cvt_scalef32_pk_f32_fp4 v[236:237], v21, 1.0
	v_cvt_scalef32_pk_f32_fp4 v[238:239], v21, 1.0 op_sel:[1,0,0]
	v_cvt_scalef32_pk_f32_fp4 v[240:241], v21, 1.0 op_sel:[0,1,0]
	v_cvt_scalef32_pk_f32_fp4 v[242:243], v21, 1.0 op_sel:[1,1,0]
	v_pk_fma_f32 v[244:245], v[228:229], v[110:111], v[244:245]
	v_pk_fma_f32 v[246:247], v[236:237], v[110:111], v[246:247]
	v_pk_fma_f32 v[244:245], v[230:231], v[112:113], v[244:245]
	v_pk_fma_f32 v[246:247], v[238:239], v[112:113], v[246:247]
	v_pk_fma_f32 v[244:245], v[232:233], v[114:115], v[244:245]
	v_pk_fma_f32 v[246:247], v[240:241], v[114:115], v[246:247]
	v_pk_fma_f32 v[244:245], v[234:235], v[116:117], v[244:245]
	v_pk_fma_f32 v[246:247], v[242:243], v[116:117], v[246:247]
	v_cvt_scalef32_pk_f32_fp4 v[228:229], v18, 1.0
	v_cvt_scalef32_pk_f32_fp4 v[230:231], v18, 1.0 op_sel:[1,0,0]
	v_cvt_scalef32_pk_f32_fp4 v[232:233], v18, 1.0 op_sel:[0,1,0]
	v_cvt_scalef32_pk_f32_fp4 v[234:235], v18, 1.0 op_sel:[1,1,0]
	v_cvt_scalef32_pk_f32_fp4 v[236:237], v22, 1.0
	v_cvt_scalef32_pk_f32_fp4 v[238:239], v22, 1.0 op_sel:[1,0,0]
	v_cvt_scalef32_pk_f32_fp4 v[240:241], v22, 1.0 op_sel:[0,1,0]
	v_cvt_scalef32_pk_f32_fp4 v[242:243], v22, 1.0 op_sel:[1,1,0]
	v_pk_fma_f32 v[244:245], v[228:229], v[118:119], v[244:245]
	v_pk_fma_f32 v[246:247], v[236:237], v[118:119], v[246:247]
	v_pk_fma_f32 v[244:245], v[230:231], v[120:121], v[244:245]
	v_pk_fma_f32 v[246:247], v[238:239], v[120:121], v[246:247]
	v_pk_fma_f32 v[244:245], v[232:233], v[122:123], v[244:245]
	v_pk_fma_f32 v[246:247], v[240:241], v[122:123], v[246:247]
	v_pk_fma_f32 v[244:245], v[234:235], v[124:125], v[244:245]
	v_pk_fma_f32 v[246:247], v[242:243], v[124:125], v[246:247]
	v_cvt_scalef32_pk_f32_fp4 v[228:229], v19, 1.0
	v_cvt_scalef32_pk_f32_fp4 v[230:231], v19, 1.0 op_sel:[1,0,0]
	v_cvt_scalef32_pk_f32_fp4 v[232:233], v19, 1.0 op_sel:[0,1,0]
	v_cvt_scalef32_pk_f32_fp4 v[234:235], v19, 1.0 op_sel:[1,1,0]
	v_cvt_scalef32_pk_f32_fp4 v[236:237], v23, 1.0
	v_cvt_scalef32_pk_f32_fp4 v[238:239], v23, 1.0 op_sel:[1,0,0]
	v_cvt_scalef32_pk_f32_fp4 v[240:241], v23, 1.0 op_sel:[0,1,0]
	v_cvt_scalef32_pk_f32_fp4 v[242:243], v23, 1.0 op_sel:[1,1,0]
	v_pk_fma_f32 v[244:245], v[228:229], v[126:127], v[244:245]
	v_pk_fma_f32 v[246:247], v[236:237], v[126:127], v[246:247]
	v_pk_fma_f32 v[244:245], v[230:231], v[128:129], v[244:245]
	v_pk_fma_f32 v[246:247], v[238:239], v[128:129], v[246:247]
	v_pk_fma_f32 v[244:245], v[232:233], v[130:131], v[244:245]
	v_pk_fma_f32 v[246:247], v[240:241], v[130:131], v[246:247]
	v_pk_fma_f32 v[244:245], v[234:235], v[132:133], v[244:245]
	v_pk_fma_f32 v[246:247], v[242:243], v[132:133], v[246:247]
	v_add_f32_e32 v190, v244, v245
	v_add_f32_e32 v191, v246, v247
	s_waitcnt vmcnt(16)
	v_cvt_scalef32_pk_f32_fp4 v[228:229], v24, 1.0
	v_cvt_scalef32_pk_f32_fp4 v[230:231], v24, 1.0 op_sel:[1,0,0]
	v_cvt_scalef32_pk_f32_fp4 v[232:233], v24, 1.0 op_sel:[0,1,0]
	v_cvt_scalef32_pk_f32_fp4 v[234:235], v24, 1.0 op_sel:[1,1,0]
	v_cvt_scalef32_pk_f32_fp4 v[236:237], v28, 1.0
	v_cvt_scalef32_pk_f32_fp4 v[238:239], v28, 1.0 op_sel:[1,0,0]
	v_cvt_scalef32_pk_f32_fp4 v[240:241], v28, 1.0 op_sel:[0,1,0]
	v_cvt_scalef32_pk_f32_fp4 v[242:243], v28, 1.0 op_sel:[1,1,0]
	v_pk_mul_f32 v[244:245], v[228:229], v[102:103]
	v_pk_mul_f32 v[246:247], v[236:237], v[102:103]
	v_pk_fma_f32 v[244:245], v[230:231], v[104:105], v[244:245]
	v_pk_fma_f32 v[246:247], v[238:239], v[104:105], v[246:247]
	v_pk_fma_f32 v[244:245], v[232:233], v[106:107], v[244:245]
	v_pk_fma_f32 v[246:247], v[240:241], v[106:107], v[246:247]
	v_pk_fma_f32 v[244:245], v[234:235], v[108:109], v[244:245]
	v_pk_fma_f32 v[246:247], v[242:243], v[108:109], v[246:247]
	v_cvt_scalef32_pk_f32_fp4 v[228:229], v25, 1.0
	v_cvt_scalef32_pk_f32_fp4 v[230:231], v25, 1.0 op_sel:[1,0,0]
	v_cvt_scalef32_pk_f32_fp4 v[232:233], v25, 1.0 op_sel:[0,1,0]
	v_cvt_scalef32_pk_f32_fp4 v[234:235], v25, 1.0 op_sel:[1,1,0]
	v_cvt_scalef32_pk_f32_fp4 v[236:237], v29, 1.0
	v_cvt_scalef32_pk_f32_fp4 v[238:239], v29, 1.0 op_sel:[1,0,0]
	v_cvt_scalef32_pk_f32_fp4 v[240:241], v29, 1.0 op_sel:[0,1,0]
	v_cvt_scalef32_pk_f32_fp4 v[242:243], v29, 1.0 op_sel:[1,1,0]
	v_pk_fma_f32 v[244:245], v[228:229], v[110:111], v[244:245]
	v_pk_fma_f32 v[246:247], v[236:237], v[110:111], v[246:247]
	v_pk_fma_f32 v[244:245], v[230:231], v[112:113], v[244:245]
	v_pk_fma_f32 v[246:247], v[238:239], v[112:113], v[246:247]
	v_pk_fma_f32 v[244:245], v[232:233], v[114:115], v[244:245]
	v_pk_fma_f32 v[246:247], v[240:241], v[114:115], v[246:247]
	v_pk_fma_f32 v[244:245], v[234:235], v[116:117], v[244:245]
	v_pk_fma_f32 v[246:247], v[242:243], v[116:117], v[246:247]
	v_cvt_scalef32_pk_f32_fp4 v[228:229], v26, 1.0
	v_cvt_scalef32_pk_f32_fp4 v[230:231], v26, 1.0 op_sel:[1,0,0]
	v_cvt_scalef32_pk_f32_fp4 v[232:233], v26, 1.0 op_sel:[0,1,0]
	v_cvt_scalef32_pk_f32_fp4 v[234:235], v26, 1.0 op_sel:[1,1,0]
	v_cvt_scalef32_pk_f32_fp4 v[236:237], v30, 1.0
	v_cvt_scalef32_pk_f32_fp4 v[238:239], v30, 1.0 op_sel:[1,0,0]
	v_cvt_scalef32_pk_f32_fp4 v[240:241], v30, 1.0 op_sel:[0,1,0]
	v_cvt_scalef32_pk_f32_fp4 v[242:243], v30, 1.0 op_sel:[1,1,0]
	v_pk_fma_f32 v[244:245], v[228:229], v[118:119], v[244:245]
	v_pk_fma_f32 v[246:247], v[236:237], v[118:119], v[246:247]
	v_pk_fma_f32 v[244:245], v[230:231], v[120:121], v[244:245]
	v_pk_fma_f32 v[246:247], v[238:239], v[120:121], v[246:247]
	v_pk_fma_f32 v[244:245], v[232:233], v[122:123], v[244:245]
	v_pk_fma_f32 v[246:247], v[240:241], v[122:123], v[246:247]
	v_pk_fma_f32 v[244:245], v[234:235], v[124:125], v[244:245]
	v_pk_fma_f32 v[246:247], v[242:243], v[124:125], v[246:247]
	v_cvt_scalef32_pk_f32_fp4 v[228:229], v27, 1.0
	v_cvt_scalef32_pk_f32_fp4 v[230:231], v27, 1.0 op_sel:[1,0,0]
	v_cvt_scalef32_pk_f32_fp4 v[232:233], v27, 1.0 op_sel:[0,1,0]
	v_cvt_scalef32_pk_f32_fp4 v[234:235], v27, 1.0 op_sel:[1,1,0]
	v_cvt_scalef32_pk_f32_fp4 v[236:237], v31, 1.0
	v_cvt_scalef32_pk_f32_fp4 v[238:239], v31, 1.0 op_sel:[1,0,0]
	v_cvt_scalef32_pk_f32_fp4 v[240:241], v31, 1.0 op_sel:[0,1,0]
	v_cvt_scalef32_pk_f32_fp4 v[242:243], v31, 1.0 op_sel:[1,1,0]
	v_pk_fma_f32 v[244:245], v[228:229], v[126:127], v[244:245]
	v_pk_fma_f32 v[246:247], v[236:237], v[126:127], v[246:247]
	v_pk_fma_f32 v[244:245], v[230:231], v[128:129], v[244:245]
	v_pk_fma_f32 v[246:247], v[238:239], v[128:129], v[246:247]
	v_pk_fma_f32 v[244:245], v[232:233], v[130:131], v[244:245]
	v_pk_fma_f32 v[246:247], v[240:241], v[130:131], v[246:247]
	v_pk_fma_f32 v[244:245], v[234:235], v[132:133], v[244:245]
	v_pk_fma_f32 v[246:247], v[242:243], v[132:133], v[246:247]
	v_add_f32_e32 v192, v244, v245
	v_add_f32_e32 v193, v246, v247
	s_waitcnt vmcnt(0)
	v_lshlrev_b32_e32 v76, 16, v68
	v_mul_f32_e32 v186, v186, v76
	v_lshlrev_b32_e32 v77, 16, v69
	v_mul_f32_e32 v187, v187, v77
	v_lshlrev_b32_e32 v76, 16, v70
	v_mul_f32_e32 v188, v188, v76
	v_lshlrev_b32_e32 v77, 16, v71
	v_mul_f32_e32 v189, v189, v77
	v_lshlrev_b32_e32 v76, 16, v72
	v_mul_f32_e32 v190, v190, v76
	v_lshlrev_b32_e32 v77, 16, v73
	v_mul_f32_e32 v191, v191, v77
	v_lshlrev_b32_e32 v76, 16, v74
	v_mul_f32_e32 v192, v192, v76
	v_lshlrev_b32_e32 v77, 16, v75
	v_mul_f32_e32 v193, v193, v77
	s_nop 1
	v_permlane32_swap_b32_e32 v186, v190
	v_permlane32_swap_b32_e32 v187, v191
	v_permlane32_swap_b32_e32 v188, v192
	v_permlane32_swap_b32_e32 v189, v193
	s_nop 0
	v_add_f32_e32 v186, v186, v190
	v_add_f32_e32 v187, v187, v191
	v_add_f32_e32 v188, v188, v192
	v_add_f32_e32 v189, v189, v193
	s_nop 1
	v_permlane16_swap_b32_e32 v186, v188
	v_permlane16_swap_b32_e32 v187, v189
	s_nop 0
	v_add_f32_e32 v186, v186, v188
	v_add_f32_e32 v187, v187, v189
	s_nop 1
	v_add_f32_dpp v248, v186, v186 row_ror:8 row_mask:0xf bank_mask:0x3
	v_add_f32_dpp v248, v187, v187 row_ror:8 row_mask:0xf bank_mask:0xc
	s_nop 1
	v_add_f32_dpp v248, v248, v248 quad_perm:[1,0,3,2] row_mask:0xf bank_mask:0xf
	s_nop 1
	v_add_f32_dpp v248, v248, v248 quad_perm:[2,3,0,1] row_mask:0xf bank_mask:0xf
	s_nop 1
	v_add_f32_dpp v248, v248, v248 row_half_mirror row_mask:0xf bank_mask:0xf
	s_waitcnt lgkmcnt(0)
	v_fma_f32 v202, |v248|, s57, 1.0
	v_mul_f32_e32 v204, v248, v248
	v_rcp_f32_e32 v202, v202
	v_mul_f32_e32 v204, 0xbf38aa3b, v204
	v_cmp_gt_f32_e32 vcc, 0, v248
	v_exp_f32_e32 v204, v204
	v_fmamk_f32 v203, v202, 0x3f07dc22, v216
	v_fmaak_f32 v203, v203, v202, 0x3f35f0e3
	v_fmaak_f32 v203, v203, v202, 0xbe11a98e
	v_fmaak_f32 v203, v203, v202, 0x3e027906
	v_mul_f32_e32 v202, v202, v203
	v_mul_f32_e32 v202, v204, v202
	v_mul_f32_e32 v203, v248, v202
	v_fma_f32 v204, -v248, v202, v248
	v_cndmask_b32_e32 v204, v204, v203, vcc
	v_mul_f32_e32 v204, v201, v204
	s_nop 1
	v_readlane_b32 s51, v204, 0
	v_readlane_b32 s64, v204, 8
	v_readlane_b32 s65, v204, 16
	v_readlane_b32 s78, v204, 24
	v_readlane_b32 s79, v204, 32
	v_readlane_b32 s82, v204, 40
	v_readlane_b32 s84, v204, 48
	v_readlane_b32 s10, v204, 56
	s_waitcnt vmcnt(14)
	v_and_b32_e32 v76, 0xffff0000, v68
	v_and_b32_e32 v77, 0xffff0000, v69
	v_mul_f32_e32 v196, s51, v76
	v_mul_f32_e32 v198, s64, v77
	v_cvt_scalef32_pk_f32_fp4 v[228:229], v36, 1.0
	v_cvt_scalef32_pk_f32_fp4 v[230:231], v36, 1.0 op_sel:[1,0,0]
	v_cvt_scalef32_pk_f32_fp4 v[232:233], v36, 1.0 op_sel:[0,1,0]
	v_cvt_scalef32_pk_f32_fp4 v[234:235], v36, 1.0 op_sel:[1,1,0]
	v_pk_fma_f32 v[178:179], v[196:197], v[228:229], v[178:179] op_sel_hi:[0,1,1]
	v_pk_fma_f32 v[184:185], v[196:197], v[230:231], v[184:185] op_sel_hi:[0,1,1]
	v_pk_fma_f32 v[182:183], v[196:197], v[232:233], v[182:183] op_sel_hi:[0,1,1]
	v_pk_fma_f32 v[180:181], v[196:197], v[234:235], v[180:181] op_sel_hi:[0,1,1]
	v_cvt_scalef32_pk_f32_fp4 v[236:237], v40, 1.0
	v_cvt_scalef32_pk_f32_fp4 v[238:239], v40, 1.0 op_sel:[1,0,0]
	v_cvt_scalef32_pk_f32_fp4 v[240:241], v40, 1.0 op_sel:[0,1,0]
	v_cvt_scalef32_pk_f32_fp4 v[242:243], v40, 1.0 op_sel:[1,1,0]
	v_pk_fma_f32 v[178:179], v[198:199], v[236:237], v[178:179] op_sel_hi:[0,1,1]
	v_pk_fma_f32 v[184:185], v[198:199], v[238:239], v[184:185] op_sel_hi:[0,1,1]
	v_pk_fma_f32 v[182:183], v[198:199], v[240:241], v[182:183] op_sel_hi:[0,1,1]
	v_pk_fma_f32 v[180:181], v[198:199], v[242:243], v[180:181] op_sel_hi:[0,1,1]
	v_cvt_scalef32_pk_f32_fp4 v[228:229], v37, 1.0
	v_cvt_scalef32_pk_f32_fp4 v[230:231], v37, 1.0 op_sel:[1,0,0]
	v_cvt_scalef32_pk_f32_fp4 v[232:233], v37, 1.0 op_sel:[0,1,0]
	v_cvt_scalef32_pk_f32_fp4 v[234:235], v37, 1.0 op_sel:[1,1,0]
	v_pk_fma_f32 v[176:177], v[196:197], v[228:229], v[176:177] op_sel_hi:[0,1,1]
	v_pk_fma_f32 v[174:175], v[196:197], v[230:231], v[174:175] op_sel_hi:[0,1,1]
	v_pk_fma_f32 v[160:161], v[196:197], v[232:233], v[160:161] op_sel_hi:[0,1,1]
	v_pk_fma_f32 v[158:159], v[196:197], v[234:235], v[158:159] op_sel_hi:[0,1,1]
	v_cvt_scalef32_pk_f32_fp4 v[236:237], v41, 1.0
	v_cvt_scalef32_pk_f32_fp4 v[238:239], v41, 1.0 op_sel:[1,0,0]
	v_cvt_scalef32_pk_f32_fp4 v[240:241], v41, 1.0 op_sel:[0,1,0]
	v_cvt_scalef32_pk_f32_fp4 v[242:243], v41, 1.0 op_sel:[1,1,0]
	v_pk_fma_f32 v[176:177], v[198:199], v[236:237], v[176:177] op_sel_hi:[0,1,1]
	v_pk_fma_f32 v[174:175], v[198:199], v[238:239], v[174:175] op_sel_hi:[0,1,1]
	v_pk_fma_f32 v[160:161], v[198:199], v[240:241], v[160:161] op_sel_hi:[0,1,1]
	v_pk_fma_f32 v[158:159], v[198:199], v[242:243], v[158:159] op_sel_hi:[0,1,1]
	v_cvt_scalef32_pk_f32_fp4 v[228:229], v38, 1.0
	v_cvt_scalef32_pk_f32_fp4 v[230:231], v38, 1.0 op_sel:[1,0,0]
	v_cvt_scalef32_pk_f32_fp4 v[232:233], v38, 1.0 op_sel:[0,1,0]
	v_cvt_scalef32_pk_f32_fp4 v[234:235], v38, 1.0 op_sel:[1,1,0]
	v_pk_fma_f32 v[156:157], v[196:197], v[228:229], v[156:157] op_sel_hi:[0,1,1]
	v_pk_fma_f32 v[154:155], v[196:197], v[230:231], v[154:155] op_sel_hi:[0,1,1]
	v_pk_fma_f32 v[152:153], v[196:197], v[232:233], v[152:153] op_sel_hi:[0,1,1]
	v_pk_fma_f32 v[150:151], v[196:197], v[234:235], v[150:151] op_sel_hi:[0,1,1]
	v_cvt_scalef32_pk_f32_fp4 v[236:237], v42, 1.0
	v_cvt_scalef32_pk_f32_fp4 v[238:239], v42, 1.0 op_sel:[1,0,0]
	v_cvt_scalef32_pk_f32_fp4 v[240:241], v42, 1.0 op_sel:[0,1,0]
	v_cvt_scalef32_pk_f32_fp4 v[242:243], v42, 1.0 op_sel:[1,1,0]
	v_pk_fma_f32 v[156:157], v[198:199], v[236:237], v[156:157] op_sel_hi:[0,1,1]
	v_pk_fma_f32 v[154:155], v[198:199], v[238:239], v[154:155] op_sel_hi:[0,1,1]
	v_pk_fma_f32 v[152:153], v[198:199], v[240:241], v[152:153] op_sel_hi:[0,1,1]
	v_pk_fma_f32 v[150:151], v[198:199], v[242:243], v[150:151] op_sel_hi:[0,1,1]
	v_cvt_scalef32_pk_f32_fp4 v[228:229], v39, 1.0
	v_cvt_scalef32_pk_f32_fp4 v[230:231], v39, 1.0 op_sel:[1,0,0]
	v_cvt_scalef32_pk_f32_fp4 v[232:233], v39, 1.0 op_sel:[0,1,0]
	v_cvt_scalef32_pk_f32_fp4 v[234:235], v39, 1.0 op_sel:[1,1,0]
	v_pk_fma_f32 v[148:149], v[196:197], v[228:229], v[148:149] op_sel_hi:[0,1,1]
	v_pk_fma_f32 v[146:147], v[196:197], v[230:231], v[146:147] op_sel_hi:[0,1,1]
	v_pk_fma_f32 v[144:145], v[196:197], v[232:233], v[144:145] op_sel_hi:[0,1,1]
	v_pk_fma_f32 v[142:143], v[196:197], v[234:235], v[142:143] op_sel_hi:[0,1,1]
	v_cvt_scalef32_pk_f32_fp4 v[236:237], v43, 1.0
	v_cvt_scalef32_pk_f32_fp4 v[238:239], v43, 1.0 op_sel:[1,0,0]
	v_cvt_scalef32_pk_f32_fp4 v[240:241], v43, 1.0 op_sel:[0,1,0]
	v_cvt_scalef32_pk_f32_fp4 v[242:243], v43, 1.0 op_sel:[1,1,0]
	v_pk_fma_f32 v[148:149], v[198:199], v[236:237], v[148:149] op_sel_hi:[0,1,1]
	v_pk_fma_f32 v[146:147], v[198:199], v[238:239], v[146:147] op_sel_hi:[0,1,1]
	v_pk_fma_f32 v[144:145], v[198:199], v[240:241], v[144:145] op_sel_hi:[0,1,1]
	v_pk_fma_f32 v[142:143], v[198:199], v[242:243], v[142:143] op_sel_hi:[0,1,1]
	s_waitcnt vmcnt(10)
	v_and_b32_e32 v76, 0xffff0000, v70
	v_and_b32_e32 v77, 0xffff0000, v71
	v_mul_f32_e32 v196, s65, v76
	v_mul_f32_e32 v198, s78, v77
	v_cvt_scalef32_pk_f32_fp4 v[228:229], v44, 1.0
	v_cvt_scalef32_pk_f32_fp4 v[230:231], v44, 1.0 op_sel:[1,0,0]
	v_cvt_scalef32_pk_f32_fp4 v[232:233], v44, 1.0 op_sel:[0,1,0]
	v_cvt_scalef32_pk_f32_fp4 v[234:235], v44, 1.0 op_sel:[1,1,0]
	v_pk_fma_f32 v[178:179], v[196:197], v[228:229], v[178:179] op_sel_hi:[0,1,1]
	v_pk_fma_f32 v[184:185], v[196:197], v[230:231], v[184:185] op_sel_hi:[0,1,1]
	v_pk_fma_f32 v[182:183], v[196:197], v[232:233], v[182:183] op_sel_hi:[0,1,1]
	v_pk_fma_f32 v[180:181], v[196:197], v[234:235], v[180:181] op_sel_hi:[0,1,1]
	v_cvt_scalef32_pk_f32_fp4 v[236:237], v48, 1.0
	v_cvt_scalef32_pk_f32_fp4 v[238:239], v48, 1.0 op_sel:[1,0,0]
	v_cvt_scalef32_pk_f32_fp4 v[240:241], v48, 1.0 op_sel:[0,1,0]
	v_cvt_scalef32_pk_f32_fp4 v[242:243], v48, 1.0 op_sel:[1,1,0]
	v_pk_fma_f32 v[178:179], v[198:199], v[236:237], v[178:179] op_sel_hi:[0,1,1]
	v_pk_fma_f32 v[184:185], v[198:199], v[238:239], v[184:185] op_sel_hi:[0,1,1]
	v_pk_fma_f32 v[182:183], v[198:199], v[240:241], v[182:183] op_sel_hi:[0,1,1]
	v_pk_fma_f32 v[180:181], v[198:199], v[242:243], v[180:181] op_sel_hi:[0,1,1]
	v_cvt_scalef32_pk_f32_fp4 v[228:229], v45, 1.0
	v_cvt_scalef32_pk_f32_fp4 v[230:231], v45, 1.0 op_sel:[1,0,0]
	v_cvt_scalef32_pk_f32_fp4 v[232:233], v45, 1.0 op_sel:[0,1,0]
	v_cvt_scalef32_pk_f32_fp4 v[234:235], v45, 1.0 op_sel:[1,1,0]
	v_pk_fma_f32 v[176:177], v[196:197], v[228:229], v[176:177] op_sel_hi:[0,1,1]
	v_pk_fma_f32 v[174:175], v[196:197], v[230:231], v[174:175] op_sel_hi:[0,1,1]
	v_pk_fma_f32 v[160:161], v[196:197], v[232:233], v[160:161] op_sel_hi:[0,1,1]
	v_pk_fma_f32 v[158:159], v[196:197], v[234:235], v[158:159] op_sel_hi:[0,1,1]
	v_cvt_scalef32_pk_f32_fp4 v[236:237], v49, 1.0
	v_cvt_scalef32_pk_f32_fp4 v[238:239], v49, 1.0 op_sel:[1,0,0]
	v_cvt_scalef32_pk_f32_fp4 v[240:241], v49, 1.0 op_sel:[0,1,0]
	v_cvt_scalef32_pk_f32_fp4 v[242:243], v49, 1.0 op_sel:[1,1,0]
	v_pk_fma_f32 v[176:177], v[198:199], v[236:237], v[176:177] op_sel_hi:[0,1,1]
	v_pk_fma_f32 v[174:175], v[198:199], v[238:239], v[174:175] op_sel_hi:[0,1,1]
	v_pk_fma_f32 v[160:161], v[198:199], v[240:241], v[160:161] op_sel_hi:[0,1,1]
	v_pk_fma_f32 v[158:159], v[198:199], v[242:243], v[158:159] op_sel_hi:[0,1,1]
	v_cvt_scalef32_pk_f32_fp4 v[228:229], v46, 1.0
	v_cvt_scalef32_pk_f32_fp4 v[230:231], v46, 1.0 op_sel:[1,0,0]
	v_cvt_scalef32_pk_f32_fp4 v[232:233], v46, 1.0 op_sel:[0,1,0]
	v_cvt_scalef32_pk_f32_fp4 v[234:235], v46, 1.0 op_sel:[1,1,0]
	v_pk_fma_f32 v[156:157], v[196:197], v[228:229], v[156:157] op_sel_hi:[0,1,1]
	v_pk_fma_f32 v[154:155], v[196:197], v[230:231], v[154:155] op_sel_hi:[0,1,1]
	v_pk_fma_f32 v[152:153], v[196:197], v[232:233], v[152:153] op_sel_hi:[0,1,1]
	v_pk_fma_f32 v[150:151], v[196:197], v[234:235], v[150:151] op_sel_hi:[0,1,1]
	v_cvt_scalef32_pk_f32_fp4 v[236:237], v50, 1.0
	v_cvt_scalef32_pk_f32_fp4 v[238:239], v50, 1.0 op_sel:[1,0,0]
	v_cvt_scalef32_pk_f32_fp4 v[240:241], v50, 1.0 op_sel:[0,1,0]
	v_cvt_scalef32_pk_f32_fp4 v[242:243], v50, 1.0 op_sel:[1,1,0]
	v_pk_fma_f32 v[156:157], v[198:199], v[236:237], v[156:157] op_sel_hi:[0,1,1]
	v_pk_fma_f32 v[154:155], v[198:199], v[238:239], v[154:155] op_sel_hi:[0,1,1]
	v_pk_fma_f32 v[152:153], v[198:199], v[240:241], v[152:153] op_sel_hi:[0,1,1]
	v_pk_fma_f32 v[150:151], v[198:199], v[242:243], v[150:151] op_sel_hi:[0,1,1]
	v_cvt_scalef32_pk_f32_fp4 v[228:229], v47, 1.0
	v_cvt_scalef32_pk_f32_fp4 v[230:231], v47, 1.0 op_sel:[1,0,0]
	v_cvt_scalef32_pk_f32_fp4 v[232:233], v47, 1.0 op_sel:[0,1,0]
	v_cvt_scalef32_pk_f32_fp4 v[234:235], v47, 1.0 op_sel:[1,1,0]
	v_pk_fma_f32 v[148:149], v[196:197], v[228:229], v[148:149] op_sel_hi:[0,1,1]
	v_pk_fma_f32 v[146:147], v[196:197], v[230:231], v[146:147] op_sel_hi:[0,1,1]
	v_pk_fma_f32 v[144:145], v[196:197], v[232:233], v[144:145] op_sel_hi:[0,1,1]
	v_pk_fma_f32 v[142:143], v[196:197], v[234:235], v[142:143] op_sel_hi:[0,1,1]
	v_cvt_scalef32_pk_f32_fp4 v[236:237], v51, 1.0
	v_cvt_scalef32_pk_f32_fp4 v[238:239], v51, 1.0 op_sel:[1,0,0]
	v_cvt_scalef32_pk_f32_fp4 v[240:241], v51, 1.0 op_sel:[0,1,0]
	v_cvt_scalef32_pk_f32_fp4 v[242:243], v51, 1.0 op_sel:[1,1,0]
	v_pk_fma_f32 v[148:149], v[198:199], v[236:237], v[148:149] op_sel_hi:[0,1,1]
	v_pk_fma_f32 v[146:147], v[198:199], v[238:239], v[146:147] op_sel_hi:[0,1,1]
	v_pk_fma_f32 v[144:145], v[198:199], v[240:241], v[144:145] op_sel_hi:[0,1,1]
	v_pk_fma_f32 v[142:143], v[198:199], v[242:243], v[142:143] op_sel_hi:[0,1,1]
	s_waitcnt vmcnt(6)
	v_and_b32_e32 v76, 0xffff0000, v72
	v_and_b32_e32 v77, 0xffff0000, v73
	v_mul_f32_e32 v196, s79, v76
	v_mul_f32_e32 v198, s82, v77
	v_cvt_scalef32_pk_f32_fp4 v[228:229], v52, 1.0
	v_cvt_scalef32_pk_f32_fp4 v[230:231], v52, 1.0 op_sel:[1,0,0]
	v_cvt_scalef32_pk_f32_fp4 v[232:233], v52, 1.0 op_sel:[0,1,0]
	v_cvt_scalef32_pk_f32_fp4 v[234:235], v52, 1.0 op_sel:[1,1,0]
	v_pk_fma_f32 v[178:179], v[196:197], v[228:229], v[178:179] op_sel_hi:[0,1,1]
	v_pk_fma_f32 v[184:185], v[196:197], v[230:231], v[184:185] op_sel_hi:[0,1,1]
	v_pk_fma_f32 v[182:183], v[196:197], v[232:233], v[182:183] op_sel_hi:[0,1,1]
	v_pk_fma_f32 v[180:181], v[196:197], v[234:235], v[180:181] op_sel_hi:[0,1,1]
	v_cvt_scalef32_pk_f32_fp4 v[236:237], v56, 1.0
	v_cvt_scalef32_pk_f32_fp4 v[238:239], v56, 1.0 op_sel:[1,0,0]
	v_cvt_scalef32_pk_f32_fp4 v[240:241], v56, 1.0 op_sel:[0,1,0]
	v_cvt_scalef32_pk_f32_fp4 v[242:243], v56, 1.0 op_sel:[1,1,0]
	v_pk_fma_f32 v[178:179], v[198:199], v[236:237], v[178:179] op_sel_hi:[0,1,1]
	v_pk_fma_f32 v[184:185], v[198:199], v[238:239], v[184:185] op_sel_hi:[0,1,1]
	v_pk_fma_f32 v[182:183], v[198:199], v[240:241], v[182:183] op_sel_hi:[0,1,1]
	v_pk_fma_f32 v[180:181], v[198:199], v[242:243], v[180:181] op_sel_hi:[0,1,1]
	v_cvt_scalef32_pk_f32_fp4 v[228:229], v53, 1.0
	v_cvt_scalef32_pk_f32_fp4 v[230:231], v53, 1.0 op_sel:[1,0,0]
	v_cvt_scalef32_pk_f32_fp4 v[232:233], v53, 1.0 op_sel:[0,1,0]
	v_cvt_scalef32_pk_f32_fp4 v[234:235], v53, 1.0 op_sel:[1,1,0]
	v_pk_fma_f32 v[176:177], v[196:197], v[228:229], v[176:177] op_sel_hi:[0,1,1]
	v_pk_fma_f32 v[174:175], v[196:197], v[230:231], v[174:175] op_sel_hi:[0,1,1]
	v_pk_fma_f32 v[160:161], v[196:197], v[232:233], v[160:161] op_sel_hi:[0,1,1]
	v_pk_fma_f32 v[158:159], v[196:197], v[234:235], v[158:159] op_sel_hi:[0,1,1]
	v_cvt_scalef32_pk_f32_fp4 v[236:237], v57, 1.0
	v_cvt_scalef32_pk_f32_fp4 v[238:239], v57, 1.0 op_sel:[1,0,0]
	v_cvt_scalef32_pk_f32_fp4 v[240:241], v57, 1.0 op_sel:[0,1,0]
	v_cvt_scalef32_pk_f32_fp4 v[242:243], v57, 1.0 op_sel:[1,1,0]
	v_pk_fma_f32 v[176:177], v[198:199], v[236:237], v[176:177] op_sel_hi:[0,1,1]
	v_pk_fma_f32 v[174:175], v[198:199], v[238:239], v[174:175] op_sel_hi:[0,1,1]
	v_pk_fma_f32 v[160:161], v[198:199], v[240:241], v[160:161] op_sel_hi:[0,1,1]
	v_pk_fma_f32 v[158:159], v[198:199], v[242:243], v[158:159] op_sel_hi:[0,1,1]
	v_cvt_scalef32_pk_f32_fp4 v[228:229], v54, 1.0
	v_cvt_scalef32_pk_f32_fp4 v[230:231], v54, 1.0 op_sel:[1,0,0]
	v_cvt_scalef32_pk_f32_fp4 v[232:233], v54, 1.0 op_sel:[0,1,0]
	v_cvt_scalef32_pk_f32_fp4 v[234:235], v54, 1.0 op_sel:[1,1,0]
	v_pk_fma_f32 v[156:157], v[196:197], v[228:229], v[156:157] op_sel_hi:[0,1,1]
	v_pk_fma_f32 v[154:155], v[196:197], v[230:231], v[154:155] op_sel_hi:[0,1,1]
	v_pk_fma_f32 v[152:153], v[196:197], v[232:233], v[152:153] op_sel_hi:[0,1,1]
	v_pk_fma_f32 v[150:151], v[196:197], v[234:235], v[150:151] op_sel_hi:[0,1,1]
	v_cvt_scalef32_pk_f32_fp4 v[236:237], v58, 1.0
	v_cvt_scalef32_pk_f32_fp4 v[238:239], v58, 1.0 op_sel:[1,0,0]
	v_cvt_scalef32_pk_f32_fp4 v[240:241], v58, 1.0 op_sel:[0,1,0]
	v_cvt_scalef32_pk_f32_fp4 v[242:243], v58, 1.0 op_sel:[1,1,0]
	v_pk_fma_f32 v[156:157], v[198:199], v[236:237], v[156:157] op_sel_hi:[0,1,1]
	v_pk_fma_f32 v[154:155], v[198:199], v[238:239], v[154:155] op_sel_hi:[0,1,1]
	v_pk_fma_f32 v[152:153], v[198:199], v[240:241], v[152:153] op_sel_hi:[0,1,1]
	v_pk_fma_f32 v[150:151], v[198:199], v[242:243], v[150:151] op_sel_hi:[0,1,1]
	v_cvt_scalef32_pk_f32_fp4 v[228:229], v55, 1.0
	v_cvt_scalef32_pk_f32_fp4 v[230:231], v55, 1.0 op_sel:[1,0,0]
	v_cvt_scalef32_pk_f32_fp4 v[232:233], v55, 1.0 op_sel:[0,1,0]
	v_cvt_scalef32_pk_f32_fp4 v[234:235], v55, 1.0 op_sel:[1,1,0]
	v_pk_fma_f32 v[148:149], v[196:197], v[228:229], v[148:149] op_sel_hi:[0,1,1]
	v_pk_fma_f32 v[146:147], v[196:197], v[230:231], v[146:147] op_sel_hi:[0,1,1]
	v_pk_fma_f32 v[144:145], v[196:197], v[232:233], v[144:145] op_sel_hi:[0,1,1]
	v_pk_fma_f32 v[142:143], v[196:197], v[234:235], v[142:143] op_sel_hi:[0,1,1]
	v_cvt_scalef32_pk_f32_fp4 v[236:237], v59, 1.0
	v_cvt_scalef32_pk_f32_fp4 v[238:239], v59, 1.0 op_sel:[1,0,0]
	v_cvt_scalef32_pk_f32_fp4 v[240:241], v59, 1.0 op_sel:[0,1,0]
	v_cvt_scalef32_pk_f32_fp4 v[242:243], v59, 1.0 op_sel:[1,1,0]
	v_pk_fma_f32 v[148:149], v[198:199], v[236:237], v[148:149] op_sel_hi:[0,1,1]
	v_pk_fma_f32 v[146:147], v[198:199], v[238:239], v[146:147] op_sel_hi:[0,1,1]
	v_pk_fma_f32 v[144:145], v[198:199], v[240:241], v[144:145] op_sel_hi:[0,1,1]
	v_pk_fma_f32 v[142:143], v[198:199], v[242:243], v[142:143] op_sel_hi:[0,1,1]
	s_waitcnt vmcnt(2)
	v_and_b32_e32 v76, 0xffff0000, v74
	v_and_b32_e32 v77, 0xffff0000, v75
	v_mul_f32_e32 v196, s84, v76
	v_mul_f32_e32 v198, s10, v77
	v_cvt_scalef32_pk_f32_fp4 v[228:229], v60, 1.0
	v_cvt_scalef32_pk_f32_fp4 v[230:231], v60, 1.0 op_sel:[1,0,0]
	v_cvt_scalef32_pk_f32_fp4 v[232:233], v60, 1.0 op_sel:[0,1,0]
	v_cvt_scalef32_pk_f32_fp4 v[234:235], v60, 1.0 op_sel:[1,1,0]
	v_pk_fma_f32 v[178:179], v[196:197], v[228:229], v[178:179] op_sel_hi:[0,1,1]
	v_pk_fma_f32 v[184:185], v[196:197], v[230:231], v[184:185] op_sel_hi:[0,1,1]
	v_pk_fma_f32 v[182:183], v[196:197], v[232:233], v[182:183] op_sel_hi:[0,1,1]
	v_pk_fma_f32 v[180:181], v[196:197], v[234:235], v[180:181] op_sel_hi:[0,1,1]
	v_cvt_scalef32_pk_f32_fp4 v[236:237], v64, 1.0
	v_cvt_scalef32_pk_f32_fp4 v[238:239], v64, 1.0 op_sel:[1,0,0]
	v_cvt_scalef32_pk_f32_fp4 v[240:241], v64, 1.0 op_sel:[0,1,0]
	v_cvt_scalef32_pk_f32_fp4 v[242:243], v64, 1.0 op_sel:[1,1,0]
	v_pk_fma_f32 v[178:179], v[198:199], v[236:237], v[178:179] op_sel_hi:[0,1,1]
	v_pk_fma_f32 v[184:185], v[198:199], v[238:239], v[184:185] op_sel_hi:[0,1,1]
	v_pk_fma_f32 v[182:183], v[198:199], v[240:241], v[182:183] op_sel_hi:[0,1,1]
	v_pk_fma_f32 v[180:181], v[198:199], v[242:243], v[180:181] op_sel_hi:[0,1,1]
	v_cvt_scalef32_pk_f32_fp4 v[228:229], v61, 1.0
	v_cvt_scalef32_pk_f32_fp4 v[230:231], v61, 1.0 op_sel:[1,0,0]
	v_cvt_scalef32_pk_f32_fp4 v[232:233], v61, 1.0 op_sel:[0,1,0]
	v_cvt_scalef32_pk_f32_fp4 v[234:235], v61, 1.0 op_sel:[1,1,0]
	v_pk_fma_f32 v[176:177], v[196:197], v[228:229], v[176:177] op_sel_hi:[0,1,1]
	v_pk_fma_f32 v[174:175], v[196:197], v[230:231], v[174:175] op_sel_hi:[0,1,1]
	v_pk_fma_f32 v[160:161], v[196:197], v[232:233], v[160:161] op_sel_hi:[0,1,1]
	v_pk_fma_f32 v[158:159], v[196:197], v[234:235], v[158:159] op_sel_hi:[0,1,1]
	v_cvt_scalef32_pk_f32_fp4 v[236:237], v65, 1.0
	v_cvt_scalef32_pk_f32_fp4 v[238:239], v65, 1.0 op_sel:[1,0,0]
	v_cvt_scalef32_pk_f32_fp4 v[240:241], v65, 1.0 op_sel:[0,1,0]
	v_cvt_scalef32_pk_f32_fp4 v[242:243], v65, 1.0 op_sel:[1,1,0]
	v_pk_fma_f32 v[176:177], v[198:199], v[236:237], v[176:177] op_sel_hi:[0,1,1]
	v_pk_fma_f32 v[174:175], v[198:199], v[238:239], v[174:175] op_sel_hi:[0,1,1]
	v_pk_fma_f32 v[160:161], v[198:199], v[240:241], v[160:161] op_sel_hi:[0,1,1]
	v_pk_fma_f32 v[158:159], v[198:199], v[242:243], v[158:159] op_sel_hi:[0,1,1]
	v_cvt_scalef32_pk_f32_fp4 v[228:229], v62, 1.0
	v_cvt_scalef32_pk_f32_fp4 v[230:231], v62, 1.0 op_sel:[1,0,0]
	v_cvt_scalef32_pk_f32_fp4 v[232:233], v62, 1.0 op_sel:[0,1,0]
	v_cvt_scalef32_pk_f32_fp4 v[234:235], v62, 1.0 op_sel:[1,1,0]
	v_pk_fma_f32 v[156:157], v[196:197], v[228:229], v[156:157] op_sel_hi:[0,1,1]
	v_pk_fma_f32 v[154:155], v[196:197], v[230:231], v[154:155] op_sel_hi:[0,1,1]
	v_pk_fma_f32 v[152:153], v[196:197], v[232:233], v[152:153] op_sel_hi:[0,1,1]
	v_pk_fma_f32 v[150:151], v[196:197], v[234:235], v[150:151] op_sel_hi:[0,1,1]
	v_cvt_scalef32_pk_f32_fp4 v[236:237], v66, 1.0
	v_cvt_scalef32_pk_f32_fp4 v[238:239], v66, 1.0 op_sel:[1,0,0]
	v_cvt_scalef32_pk_f32_fp4 v[240:241], v66, 1.0 op_sel:[0,1,0]
	v_cvt_scalef32_pk_f32_fp4 v[242:243], v66, 1.0 op_sel:[1,1,0]
	v_pk_fma_f32 v[156:157], v[198:199], v[236:237], v[156:157] op_sel_hi:[0,1,1]
	v_pk_fma_f32 v[154:155], v[198:199], v[238:239], v[154:155] op_sel_hi:[0,1,1]
	v_pk_fma_f32 v[152:153], v[198:199], v[240:241], v[152:153] op_sel_hi:[0,1,1]
	v_pk_fma_f32 v[150:151], v[198:199], v[242:243], v[150:151] op_sel_hi:[0,1,1]
	v_cvt_scalef32_pk_f32_fp4 v[228:229], v63, 1.0
	v_cvt_scalef32_pk_f32_fp4 v[230:231], v63, 1.0 op_sel:[1,0,0]
	v_cvt_scalef32_pk_f32_fp4 v[232:233], v63, 1.0 op_sel:[0,1,0]
	v_cvt_scalef32_pk_f32_fp4 v[234:235], v63, 1.0 op_sel:[1,1,0]
	v_pk_fma_f32 v[148:149], v[196:197], v[228:229], v[148:149] op_sel_hi:[0,1,1]
	v_pk_fma_f32 v[146:147], v[196:197], v[230:231], v[146:147] op_sel_hi:[0,1,1]
	v_pk_fma_f32 v[144:145], v[196:197], v[232:233], v[144:145] op_sel_hi:[0,1,1]
	v_pk_fma_f32 v[142:143], v[196:197], v[234:235], v[142:143] op_sel_hi:[0,1,1]
	v_cvt_scalef32_pk_f32_fp4 v[236:237], v67, 1.0
	v_cvt_scalef32_pk_f32_fp4 v[238:239], v67, 1.0 op_sel:[1,0,0]
	v_cvt_scalef32_pk_f32_fp4 v[240:241], v67, 1.0 op_sel:[0,1,0]
	v_cvt_scalef32_pk_f32_fp4 v[242:243], v67, 1.0 op_sel:[1,1,0]
	v_pk_fma_f32 v[148:149], v[198:199], v[236:237], v[148:149] op_sel_hi:[0,1,1]
	v_pk_fma_f32 v[146:147], v[198:199], v[238:239], v[146:147] op_sel_hi:[0,1,1]
	v_pk_fma_f32 v[144:145], v[198:199], v[240:241], v[144:145] op_sel_hi:[0,1,1]
	v_pk_fma_f32 v[142:143], v[198:199], v[242:243], v[142:143] op_sel_hi:[0,1,1]
.Lge_epi:
	s_ashr_i32 s2, s44, 13
	s_lshl_b64 s[0:1], s[44:45], 12
	v_lshlrev_b32_e32 v78, 4, v80
	v_add_u32_e32 v78, 0x4000, v78
	s_lshl_b32 s10, s2, 13
	v_add_u32_e32 v79, s10, v78
	ds_read_b128 v[36:39], v79 offset:0
	ds_read_b128 v[40:43], v79 offset:1024
	ds_read_b128 v[44:47], v79 offset:2048
	ds_read_b128 v[48:51], v79 offset:3072
	ds_read_b128 v[52:55], v79 offset:4096
	ds_read_b128 v[56:59], v79 offset:5120
	ds_read_b128 v[60:63], v79 offset:6144
	ds_read_b128 v[64:67], v79 offset:7168
	s_lshl_b32 s10, s2, 14
	v_add_u32_e32 v78, s10, v78
	s_waitcnt lgkmcnt(0)
	v_lshlrev_b32_e32 v70, 16, v98
	v_and_b32_e32 v71, 0xffff0000, v98
	v_pk_fma_f32 v[124:125], v[148:149], v[60:61], v[70:71]
	v_lshlrev_b32_e32 v70, 16, v99
	v_and_b32_e32 v71, 0xffff0000, v99
	v_pk_fma_f32 v[126:127], v[146:147], v[62:63], v[70:71]
	v_lshlrev_b32_e32 v70, 16, v100
	v_and_b32_e32 v71, 0xffff0000, v100
	v_pk_fma_f32 v[128:129], v[144:145], v[64:65], v[70:71]
	v_lshlrev_b32_e32 v70, 16, v101
	v_and_b32_e32 v71, 0xffff0000, v101
	v_pk_fma_f32 v[130:131], v[142:143], v[66:67], v[70:71]
	v_lshlrev_b32_e32 v70, 16, v32
	v_and_b32_e32 v71, 0xffff0000, v32
	v_pk_fma_f32 v[100:101], v[178:179], v[36:37], v[70:71]
	v_lshlrev_b32_e32 v70, 16, v33
	v_and_b32_e32 v71, 0xffff0000, v33
	v_pk_fma_f32 v[102:103], v[184:185], v[38:39], v[70:71]
	v_lshlrev_b32_e32 v70, 16, v34
	v_and_b32_e32 v71, 0xffff0000, v34
	v_pk_fma_f32 v[104:105], v[182:183], v[40:41], v[70:71]
	v_lshlrev_b32_e32 v70, 16, v35
	v_and_b32_e32 v71, 0xffff0000, v35
	v_pk_fma_f32 v[106:107], v[180:181], v[42:43], v[70:71]
	v_lshlrev_b32_e32 v70, 16, v138
	v_and_b32_e32 v71, 0xffff0000, v138
	v_pk_fma_f32 v[108:109], v[176:177], v[44:45], v[70:71]
	v_lshlrev_b32_e32 v70, 16, v139
	v_and_b32_e32 v71, 0xffff0000, v139
	v_pk_fma_f32 v[110:111], v[174:175], v[46:47], v[70:71]
	v_lshlrev_b32_e32 v70, 16, v140
	v_and_b32_e32 v71, 0xffff0000, v140
	v_pk_fma_f32 v[112:113], v[160:161], v[48:49], v[70:71]
	v_lshlrev_b32_e32 v70, 16, v141
	v_and_b32_e32 v71, 0xffff0000, v141
	v_pk_fma_f32 v[114:115], v[158:159], v[50:51], v[70:71]
	v_lshlrev_b32_e32 v70, 16, v206
	v_and_b32_e32 v71, 0xffff0000, v206
	v_pk_fma_f32 v[116:117], v[156:157], v[52:53], v[70:71]
	v_lshlrev_b32_e32 v70, 16, v207
	v_and_b32_e32 v71, 0xffff0000, v207
	v_pk_fma_f32 v[118:119], v[154:155], v[54:55], v[70:71]
	v_lshlrev_b32_e32 v70, 16, v208
	v_and_b32_e32 v71, 0xffff0000, v208
	v_pk_fma_f32 v[120:121], v[152:153], v[56:57], v[70:71]
	v_lshlrev_b32_e32 v70, 16, v209
	v_and_b32_e32 v71, 0xffff0000, v209
	v_pk_fma_f32 v[122:123], v[150:151], v[58:59], v[70:71]
	v_pk_mul_f32 v[72:73], v[100:101], v[100:101]
	v_pk_fma_f32 v[72:73], v[102:103], v[102:103], v[72:73]
	v_pk_fma_f32 v[72:73], v[104:105], v[104:105], v[72:73]
	v_pk_fma_f32 v[72:73], v[106:107], v[106:107], v[72:73]
	v_pk_fma_f32 v[72:73], v[108:109], v[108:109], v[72:73]
	v_pk_fma_f32 v[72:73], v[110:111], v[110:111], v[72:73]
	v_pk_fma_f32 v[72:73], v[112:113], v[112:113], v[72:73]
	v_pk_fma_f32 v[72:73], v[114:115], v[114:115], v[72:73]
	v_pk_fma_f32 v[72:73], v[116:117], v[116:117], v[72:73]
	v_pk_fma_f32 v[72:73], v[118:119], v[118:119], v[72:73]
	v_pk_fma_f32 v[72:73], v[120:121], v[120:121], v[72:73]
	v_pk_fma_f32 v[72:73], v[122:123], v[122:123], v[72:73]
	v_pk_fma_f32 v[72:73], v[124:125], v[124:125], v[72:73]
	v_pk_fma_f32 v[72:73], v[126:127], v[126:127], v[72:73]
	v_pk_fma_f32 v[72:73], v[128:129], v[128:129], v[72:73]
	v_pk_fma_f32 v[72:73], v[130:131], v[130:131], v[72:73]
	v_add_f32_e32 v72, v72, v73
	s_and_b64 vcc, exec, s[52:53]
	s_cbranch_vccz .Lge_noxc
	v_cvt_pk_bf16_f32 v36, v100, v101
	v_cvt_pk_bf16_f32 v37, v102, v103
	v_cvt_pk_bf16_f32 v38, v104, v105
	v_cvt_pk_bf16_f32 v39, v106, v107
	v_cvt_pk_bf16_f32 v40, v108, v109
	v_cvt_pk_bf16_f32 v41, v110, v111
	v_cvt_pk_bf16_f32 v42, v112, v113
	v_cvt_pk_bf16_f32 v43, v114, v115
	v_cvt_pk_bf16_f32 v44, v116, v117
	v_cvt_pk_bf16_f32 v45, v118, v119
	v_cvt_pk_bf16_f32 v46, v120, v121
	v_cvt_pk_bf16_f32 v47, v122, v123
	v_cvt_pk_bf16_f32 v48, v124, v125
	v_cvt_pk_bf16_f32 v49, v126, v127
	v_cvt_pk_bf16_f32 v50, v128, v129
	v_cvt_pk_bf16_f32 v51, v130, v131
	v_lshl_add_u64 v[68:69], v[94:95], 0, s[0:1]
	global_store_dwordx4 v[68:69], v[36:39], off offset:0
	global_store_dwordx4 v[68:69], v[40:43], off offset:16
	global_store_dwordx4 v[68:69], v[44:47], off offset:32
	global_store_dwordx4 v[68:69], v[48:51], off offset:48
.Lge_noxc:
	v_mov_b32_e32 v73, v97
	s_nop 0
	v_add_f32_dpp v72, v72, v72 quad_perm:[1,0,3,2] row_mask:0xf bank_mask:0xf bound_ctrl:1
	s_nop 1
	v_add_f32_dpp v72, v72, v72 quad_perm:[2,3,0,1] row_mask:0xf bank_mask:0xf bound_ctrl:1
	s_nop 1
	v_add_f32_dpp v72, v72, v72 row_half_mirror row_mask:0xf bank_mask:0xf bound_ctrl:1
	s_nop 1
	v_add_f32_dpp v72, v72, v72 row_mirror row_mask:0xf bank_mask:0xf bound_ctrl:1
	s_nop 1
	v_mov_b32_dpp v73, v72 row_bcast:15 row_mask:0xa bank_mask:0xf
	v_add_f32_e32 v72, v72, v73
	v_mov_b32_e32 v73, v97
	s_nop 1
	v_mov_b32_dpp v73, v72 row_bcast:31 row_mask:0xc bank_mask:0xf
	v_add_f32_e32 v72, v72, v73
	s_nop 0
	v_readlane_b32 s4, v72, 63
	s_nop 1
	v_fma_f32 v76, s4, v217, v205
	v_mul_f32_e32 v77, 0x4b800000, v76
	v_cmp_gt_f32_e32 vcc, s17, v76
	s_nop 1
	v_cndmask_b32_e32 v76, v76, v77, vcc
	v_rsq_f32_e32 v76, v76
	s_nop 0
	v_mul_f32_e32 v77, 0x45800000, v76
	v_cndmask_b32_e32 v76, v76, v77, vcc
	s_and_b64 vcc, exec, s[52:53]
	s_cbranch_vccz .Lge_final
	ds_read_b128 v[36:39], v78 offset:16384
	ds_read_b128 v[40:43], v78 offset:17408
	ds_read_b128 v[44:47], v78 offset:18432
	ds_read_b128 v[48:51], v78 offset:19456
	ds_read_b128 v[52:55], v78 offset:20480
	ds_read_b128 v[56:59], v78 offset:21504
	ds_read_b128 v[60:63], v78 offset:22528
	ds_read_b128 v[64:67], v78 offset:23552
	ds_read_b128 v[0:3], v78 offset:24576
	ds_read_b128 v[4:7], v78 offset:25600
	ds_read_b128 v[8:11], v78 offset:26624
	ds_read_b128 v[12:15], v78 offset:27648
	ds_read_b128 v[16:19], v78 offset:28672
	ds_read_b128 v[20:23], v78 offset:29696
	ds_read_b128 v[24:27], v78 offset:30720
	ds_read_b128 v[28:31], v78 offset:31744
	s_waitcnt lgkmcnt(0)
	v_pk_mul_f32 v[36:37], v[36:37], v[76:77] op_sel_hi:[1,0]
	v_pk_mul_f32 v[38:39], v[38:39], v[76:77] op_sel_hi:[1,0]
	v_pk_mul_f32 v[40:41], v[40:41], v[76:77] op_sel_hi:[1,0]
	v_pk_mul_f32 v[42:43], v[42:43], v[76:77] op_sel_hi:[1,0]
	v_pk_mul_f32 v[44:45], v[44:45], v[76:77] op_sel_hi:[1,0]
	v_pk_mul_f32 v[46:47], v[46:47], v[76:77] op_sel_hi:[1,0]
	v_pk_mul_f32 v[48:49], v[48:49], v[76:77] op_sel_hi:[1,0]
	v_pk_mul_f32 v[50:51], v[50:51], v[76:77] op_sel_hi:[1,0]
	v_pk_mul_f32 v[52:53], v[52:53], v[76:77] op_sel_hi:[1,0]
	v_pk_mul_f32 v[54:55], v[54:55], v[76:77] op_sel_hi:[1,0]
	v_pk_mul_f32 v[56:57], v[56:57], v[76:77] op_sel_hi:[1,0]
	v_pk_mul_f32 v[58:59], v[58:59], v[76:77] op_sel_hi:[1,0]
	v_pk_mul_f32 v[60:61], v[60:61], v[76:77] op_sel_hi:[1,0]
	v_pk_mul_f32 v[62:63], v[62:63], v[76:77] op_sel_hi:[1,0]
	v_pk_mul_f32 v[64:65], v[64:65], v[76:77] op_sel_hi:[1,0]
	v_pk_mul_f32 v[66:67], v[66:67], v[76:77] op_sel_hi:[1,0]
	v_pk_fma_f32 v[0:1], v[100:101], v[36:37], v[0:1]
	v_pk_fma_f32 v[2:3], v[102:103], v[38:39], v[2:3]
	v_pk_fma_f32 v[4:5], v[104:105], v[40:41], v[4:5]
	v_pk_fma_f32 v[6:7], v[106:107], v[42:43], v[6:7]
	v_pk_fma_f32 v[8:9], v[108:109], v[44:45], v[8:9]
	v_pk_fma_f32 v[10:11], v[110:111], v[46:47], v[10:11]
	v_pk_fma_f32 v[12:13], v[112:113], v[48:49], v[12:13]
	v_pk_fma_f32 v[14:15], v[114:115], v[50:51], v[14:15]
	v_pk_fma_f32 v[16:17], v[116:117], v[52:53], v[16:17]
	v_pk_fma_f32 v[18:19], v[118:119], v[54:55], v[18:19]
	v_pk_fma_f32 v[20:21], v[120:121], v[56:57], v[20:21]
	v_pk_fma_f32 v[22:23], v[122:123], v[58:59], v[22:23]
	v_pk_fma_f32 v[24:25], v[124:125], v[60:61], v[24:25]
	v_pk_fma_f32 v[26:27], v[126:127], v[62:63], v[26:27]
	v_pk_fma_f32 v[28:29], v[128:129], v[64:65], v[28:29]
	v_pk_fma_f32 v[30:31], v[130:131], v[66:67], v[30:31]
	v_cvt_pk_bf16_f32 v36, v0, v1
	v_cvt_pk_bf16_f32 v37, v2, v3
	v_cvt_pk_bf16_f32 v38, v4, v5
	v_cvt_pk_bf16_f32 v39, v6, v7
	v_cvt_pk_bf16_f32 v40, v8, v9
	v_cvt_pk_bf16_f32 v41, v10, v11
	v_cvt_pk_bf16_f32 v42, v12, v13
	v_cvt_pk_bf16_f32 v43, v14, v15
	v_cvt_pk_bf16_f32 v44, v16, v17
	v_cvt_pk_bf16_f32 v45, v18, v19
	v_cvt_pk_bf16_f32 v46, v20, v21
	v_cvt_pk_bf16_f32 v47, v22, v23
	v_cvt_pk_bf16_f32 v48, v24, v25
	v_cvt_pk_bf16_f32 v49, v26, v27
	v_cvt_pk_bf16_f32 v50, v28, v29
	v_cvt_pk_bf16_f32 v51, v30, v31
	v_lshl_add_u64 v[68:69], v[84:85], 0, s[0:1]
	global_store_dwordx4 v[68:69], v[36:39], off offset:0
	global_store_dwordx4 v[68:69], v[40:43], off offset:16
	global_store_dwordx4 v[68:69], v[44:47], off offset:32
	global_store_dwordx4 v[68:69], v[48:51], off offset:48
	s_nop 1
	s_and_b64 vcc, exec, s[54:55]
	s_cbranch_vccz .LBB0_1404
	ds_read_b128 v[36:39], v78 offset:49152
	ds_read_b128 v[40:43], v78 offset:50176
	ds_read_b128 v[44:47], v78 offset:51200
	ds_read_b128 v[48:51], v78 offset:52224
	ds_read_b128 v[52:55], v78 offset:53248
	ds_read_b128 v[56:59], v78 offset:54272
	ds_read_b128 v[60:63], v78 offset:55296
	ds_read_b128 v[64:67], v78 offset:56320
	ds_read_b128 v[0:3], v78 offset:57344
	ds_read_b128 v[4:7], v78 offset:58368
	ds_read_b128 v[8:11], v78 offset:59392
	ds_read_b128 v[12:15], v78 offset:60416
	ds_read_b128 v[16:19], v78 offset:61440
	ds_read_b128 v[20:23], v78 offset:62464
	ds_read_b128 v[24:27], v78 offset:63488
	ds_read_b128 v[28:31], v78 offset:64512
	s_waitcnt lgkmcnt(0)
	v_pk_mul_f32 v[36:37], v[36:37], v[76:77] op_sel_hi:[1,0]
	v_pk_mul_f32 v[38:39], v[38:39], v[76:77] op_sel_hi:[1,0]
	v_pk_mul_f32 v[40:41], v[40:41], v[76:77] op_sel_hi:[1,0]
	v_pk_mul_f32 v[42:43], v[42:43], v[76:77] op_sel_hi:[1,0]
	v_pk_mul_f32 v[44:45], v[44:45], v[76:77] op_sel_hi:[1,0]
	v_pk_mul_f32 v[46:47], v[46:47], v[76:77] op_sel_hi:[1,0]
	v_pk_mul_f32 v[48:49], v[48:49], v[76:77] op_sel_hi:[1,0]
	v_pk_mul_f32 v[50:51], v[50:51], v[76:77] op_sel_hi:[1,0]
	v_pk_mul_f32 v[52:53], v[52:53], v[76:77] op_sel_hi:[1,0]
	v_pk_mul_f32 v[54:55], v[54:55], v[76:77] op_sel_hi:[1,0]
	v_pk_mul_f32 v[56:57], v[56:57], v[76:77] op_sel_hi:[1,0]
	v_pk_mul_f32 v[58:59], v[58:59], v[76:77] op_sel_hi:[1,0]
	v_pk_mul_f32 v[60:61], v[60:61], v[76:77] op_sel_hi:[1,0]
	v_pk_mul_f32 v[62:63], v[62:63], v[76:77] op_sel_hi:[1,0]
	v_pk_mul_f32 v[64:65], v[64:65], v[76:77] op_sel_hi:[1,0]
	v_pk_mul_f32 v[66:67], v[66:67], v[76:77] op_sel_hi:[1,0]
	v_pk_fma_f32 v[0:1], v[100:101], v[36:37], v[0:1]
	v_pk_fma_f32 v[2:3], v[102:103], v[38:39], v[2:3]
	v_pk_fma_f32 v[4:5], v[104:105], v[40:41], v[4:5]
	v_pk_fma_f32 v[6:7], v[106:107], v[42:43], v[6:7]
	v_pk_fma_f32 v[8:9], v[108:109], v[44:45], v[8:9]
	v_pk_fma_f32 v[10:11], v[110:111], v[46:47], v[10:11]
	v_pk_fma_f32 v[12:13], v[112:113], v[48:49], v[12:13]
	v_pk_fma_f32 v[14:15], v[114:115], v[50:51], v[14:15]
	v_pk_fma_f32 v[16:17], v[116:117], v[52:53], v[16:17]
	v_pk_fma_f32 v[18:19], v[118:119], v[54:55], v[18:19]
	v_pk_fma_f32 v[20:21], v[120:121], v[56:57], v[20:21]
	v_pk_fma_f32 v[22:23], v[122:123], v[58:59], v[22:23]
	v_pk_fma_f32 v[24:25], v[124:125], v[60:61], v[24:25]
	v_pk_fma_f32 v[26:27], v[126:127], v[62:63], v[26:27]
	v_pk_fma_f32 v[28:29], v[128:129], v[64:65], v[28:29]
	v_pk_fma_f32 v[30:31], v[130:131], v[66:67], v[30:31]
	v_cvt_pk_bf16_f32 v36, v0, v1
	v_cvt_pk_bf16_f32 v37, v2, v3
	v_cvt_pk_bf16_f32 v38, v4, v5
	v_cvt_pk_bf16_f32 v39, v6, v7
	v_cvt_pk_bf16_f32 v40, v8, v9
	v_cvt_pk_bf16_f32 v41, v10, v11
	v_cvt_pk_bf16_f32 v42, v12, v13
	v_cvt_pk_bf16_f32 v43, v14, v15
	v_cvt_pk_bf16_f32 v44, v16, v17
	v_cvt_pk_bf16_f32 v45, v18, v19
	v_cvt_pk_bf16_f32 v46, v20, v21
	v_cvt_pk_bf16_f32 v47, v22, v23
	v_cvt_pk_bf16_f32 v48, v24, v25
	v_cvt_pk_bf16_f32 v49, v26, v27
	v_cvt_pk_bf16_f32 v50, v28, v29
	v_cvt_pk_bf16_f32 v51, v30, v31
	v_lshl_add_u64 v[68:69], v[86:87], 0, s[0:1]
	global_store_dwordx4 v[68:69], v[36:39], off offset:0
	global_store_dwordx4 v[68:69], v[40:43], off offset:16
	global_store_dwordx4 v[68:69], v[44:47], off offset:32
	global_store_dwordx4 v[68:69], v[48:51], off offset:48
	s_nop 1
	s_branch .LBB0_1404
.Lge_final:
	s_load_dwordx2 s[40:41], s[36:37], 0xd0
	v_lshlrev_b32_e32 v78, 4, v80
	v_add_u32_e32 v78, 0x4000, v78
	ds_read_b128 v[36:39], v78 offset:16384
	ds_read_b128 v[40:43], v78 offset:17408
	ds_read_b128 v[44:47], v78 offset:18432
	ds_read_b128 v[48:51], v78 offset:19456
	ds_read_b128 v[52:55], v78 offset:20480
	ds_read_b128 v[56:59], v78 offset:21504
	ds_read_b128 v[60:63], v78 offset:22528
	ds_read_b128 v[64:67], v78 offset:23552
	s_lshl_b64 s[0:1], s[44:45], 13
	v_lshlrev_b32_e32 v79, 7, v80
	s_waitcnt lgkmcnt(0)
	s_add_u32 s0, s40, s0
	s_addc_u32 s1, s41, s1
	v_pk_mul_f32 v[100:101], v[100:101], v[76:77] op_sel_hi:[1,0]
	v_pk_mul_f32 v[102:103], v[102:103], v[76:77] op_sel_hi:[1,0]
	v_pk_mul_f32 v[104:105], v[104:105], v[76:77] op_sel_hi:[1,0]
	v_pk_mul_f32 v[106:107], v[106:107], v[76:77] op_sel_hi:[1,0]
	v_pk_mul_f32 v[108:109], v[108:109], v[76:77] op_sel_hi:[1,0]
	v_pk_mul_f32 v[110:111], v[110:111], v[76:77] op_sel_hi:[1,0]
	v_pk_mul_f32 v[112:113], v[112:113], v[76:77] op_sel_hi:[1,0]
	v_pk_mul_f32 v[114:115], v[114:115], v[76:77] op_sel_hi:[1,0]
	v_pk_mul_f32 v[116:117], v[116:117], v[76:77] op_sel_hi:[1,0]
	v_pk_mul_f32 v[118:119], v[118:119], v[76:77] op_sel_hi:[1,0]
	v_pk_mul_f32 v[120:121], v[120:121], v[76:77] op_sel_hi:[1,0]
	v_pk_mul_f32 v[122:123], v[122:123], v[76:77] op_sel_hi:[1,0]
	v_pk_mul_f32 v[124:125], v[124:125], v[76:77] op_sel_hi:[1,0]
	v_pk_mul_f32 v[126:127], v[126:127], v[76:77] op_sel_hi:[1,0]
	v_pk_mul_f32 v[128:129], v[128:129], v[76:77] op_sel_hi:[1,0]
	v_pk_mul_f32 v[130:131], v[130:131], v[76:77] op_sel_hi:[1,0]
	v_pk_mul_f32 v[100:101], v[100:101], v[36:37]
	v_pk_mul_f32 v[102:103], v[102:103], v[38:39]
	v_pk_mul_f32 v[104:105], v[104:105], v[40:41]
	v_pk_mul_f32 v[106:107], v[106:107], v[42:43]
	v_pk_mul_f32 v[108:109], v[108:109], v[44:45]
	v_pk_mul_f32 v[110:111], v[110:111], v[46:47]
	v_pk_mul_f32 v[112:113], v[112:113], v[48:49]
	v_pk_mul_f32 v[114:115], v[114:115], v[50:51]
	v_pk_mul_f32 v[116:117], v[116:117], v[52:53]
	v_pk_mul_f32 v[118:119], v[118:119], v[54:55]
	v_pk_mul_f32 v[120:121], v[120:121], v[56:57]
	v_pk_mul_f32 v[122:123], v[122:123], v[58:59]
	v_pk_mul_f32 v[124:125], v[124:125], v[60:61]
	v_pk_mul_f32 v[126:127], v[126:127], v[62:63]
	v_pk_mul_f32 v[128:129], v[128:129], v[64:65]
	v_pk_mul_f32 v[130:131], v[130:131], v[66:67]
	global_store_dwordx4 v79, v[100:103], s[0:1] offset:0
	global_store_dwordx4 v79, v[104:107], s[0:1] offset:16
	global_store_dwordx4 v79, v[108:111], s[0:1] offset:32
	global_store_dwordx4 v79, v[112:115], s[0:1] offset:48
	global_store_dwordx4 v79, v[116:119], s[0:1] offset:64
	global_store_dwordx4 v79, v[120:123], s[0:1] offset:80
	global_store_dwordx4 v79, v[124:127], s[0:1] offset:96
	global_store_dwordx4 v79, v[128:131], s[0:1] offset:112
	s_nop 1
	s_branch .LBB0_1404
